# speedup vs baseline: 1.0104x; 1.0104x over previous
.Lk_15:
	global_load_dword v66, v[62:63], off offset:4
	global_load_dword v67, v[62:63], off offset:260
	global_load_dword v68, v[62:63], off offset:516
	global_load_dword v69, v[62:63], off offset:772
	global_load_dword v70, v[64:65], off offset:4
	global_load_dword v71, v[64:65], off offset:260
	global_load_dword v72, v[64:65], off offset:516
	global_load_dword v73, v[64:65], off offset:772
	v_and_b32_e32 v62, 15, v0
	s_mov_b32 s8, 0x4038aa3b
	s_waitcnt vmcnt(11)
	v_pk_mul_f32 v[38:39], v[50:51], v[38:39]
	v_lshlrev_b32_e32 v57, 2, v1
	s_lshl_b32 s10, s34, 8
	v_lshlrev_b32_e32 v1, 4, v62
	v_pk_add_f32 v[52:53], v[52:53], v[54:55]
	v_pk_add_f32 v[54:55], v[58:59], v[60:61]
	s_mov_b32 s9, 0xbfb8aa3b
	s_waitcnt vmcnt(10)
	v_pk_mul_f32 v[46:47], v[50:51], v[46:47]
	v_pk_mul_f32 v[48:49], v[50:51], v[48:49]
	v_pk_mul_f32 v[40:41], v[50:51], v[40:41]
	s_waitcnt vmcnt(8)
	v_pk_mul_f32 v[42:43], v[50:51], v[42:43]
	v_pk_mul_f32 v[44:45], v[50:51], v[44:45]
	v_pk_mul_f32 v[34:35], v[50:51], v[34:35]
	v_pk_mul_f32 v[36:37], v[50:51], v[36:37]
	v_pk_mul_f32 v[30:31], v[50:51], v[30:31]
	v_pk_mul_f32 v[32:33], v[50:51], v[32:33]
	v_pk_mul_f32 v[18:19], v[50:51], v[18:19]
	v_pk_mul_f32 v[58:59], v[50:51], v[20:21]
	v_pk_mul_f32 v[60:61], v[50:51], v[26:27]
	v_pk_mul_f32 v[64:65], v[50:51], v[28:29]
	v_pk_mul_f32 v[74:75], v[50:51], v[22:23]
	v_pk_mul_f32 v[50:51], v[50:51], v[24:25]
	v_cvt_pk_f16_f32 v24, v38, v39
	v_or3_b32 v38, v1, v57, s10
	v_lshlrev_b32_e32 v82, 4, v80
	s_and_b64 vcc, exec, s[6:7]
	s_mov_b32 s6, s9
	v_cvt_pk_f16_f32 v25, v40, v41
	v_add_u32_e32 v81, 0x23280, v38
	s_mov_b64 s[4:5], -1
	v_pk_mul_f32 v[20:21], v[54:55], s[8:9]
	v_cvt_pk_f16_f32 v22, v46, v47
	v_cvt_pk_f16_f32 v23, v48, v49
	v_cvt_pk_f16_f32 v26, v42, v43
	v_cvt_pk_f16_f32 v27, v44, v45
	v_cvt_pk_f16_f32 v28, v34, v35
	v_cvt_pk_f16_f32 v29, v36, v37
	v_cvt_pk_f16_f32 v30, v30, v31
	v_cvt_pk_f16_f32 v31, v32, v33
	v_cvt_pk_f16_f32 v32, v18, v19
	v_cvt_pk_f16_f32 v33, v58, v59
	v_cvt_pk_f16_f32 v34, v60, v61
	v_cvt_pk_f16_f32 v35, v64, v65
	v_cvt_pk_f16_f32 v36, v74, v75
	v_cvt_pk_f16_f32 v37, v50, v51
	v_add_u32_e32 v75, 0x23280, v82
	v_pk_mul_f32 v[18:19], v[52:53], s[6:7] op_sel_hi:[1,0]
	s_waitcnt lgkmcnt(0)
	s_barrier
	s_waitcnt vmcnt(2)
	v_pk_add_f32 v[38:39], v[66:67], v[70:71]
	s_nop 0
	v_pk_mul_f32 v[38:39], v[38:39], s[6:7] op_sel_hi:[1,0]
	s_waitcnt vmcnt(0)
	v_pk_add_f32 v[40:41], v[68:69], v[72:73]
	s_nop 0
	v_pk_mul_f32 v[40:41], v[40:41], s[8:9]
	s_cbranch_vccz .Lk_134
	s_setprio 0
	v_lshrrev_b32_e32 v42, 4, v80
	v_lshlrev_b32_e32 v42, 5, v42
	global_load_dwordx4 v[44:47], v42, s[18:19]
	global_load_dwordx4 v[48:51], v42, s[18:19] offset:16
	global_load_dwordx4 v[52:55], v42, s[18:19] offset:128
	global_load_dwordx4 v[56:59], v42, s[18:19] offset:144
	s_load_dword s28, s[20:21], 0x0
	v_and_b32_e32 v43, 15, v80
	v_cmp_eq_u32_e32 vcc, 1, v43
	v_cmp_eq_u32_e64 s[4:5], 0, v43
	v_cmp_gt_u32_e64 s[30:31], 16, v80
	v_lshl_or_b32 v124, s3, 4, v43
	v_mul_u32_u24_e32 v124, 0x708, v124
	v_lshlrev_b32_e32 v74, 2, v43
	v_add_u32_e32 v74, 0x1c200, v74
	v_mov_b32_e32 v72, 0x3fe10966
	v_mov_b32_e32 v73, 0xbfe10966
	v_mov_b32_e32 v92, 0xc038aa3b
	v_mov_b32_e32 v93, 0xc038aa3b
	s_mov_b32 s8, 0x4038aa3b
	s_mov_b32 s9, 0
	v_mov_b32_e32 v64, 0
	v_mov_b32_e32 v65, 0
	s_mov_b32 s12, 4
	s_waitcnt vmcnt(0) lgkmcnt(0)
	v_cvt_f16_f32_e32 v60, v44
	v_cvt_f32_f16_e32 v61, v60
	v_sub_f32_e32 v61, v44, v61
	v_cvt_f16_f32_e32 v61, v61
	v_cndmask_b32_e32 v61, 0, v61, vcc
	v_cndmask_b32_e64 v94, v61, v60, s[4:5]
	v_cvt_f16_f32_e32 v60, v45
	v_cvt_f32_f16_e32 v61, v60
	v_sub_f32_e32 v61, v45, v61
	v_cvt_f16_f32_e32 v61, v61
	v_cndmask_b32_e32 v61, 0, v61, vcc
	v_cndmask_b32_e64 v95, v61, v60, s[4:5]
	v_cvt_f16_f32_e32 v60, v46
	v_cvt_f32_f16_e32 v61, v60
	v_sub_f32_e32 v61, v46, v61
	v_cvt_f16_f32_e32 v61, v61
	v_cndmask_b32_e32 v61, 0, v61, vcc
	v_cndmask_b32_e64 v96, v61, v60, s[4:5]
	v_cvt_f16_f32_e32 v60, v47
	v_cvt_f32_f16_e32 v61, v60
	v_sub_f32_e32 v61, v47, v61
	v_cvt_f16_f32_e32 v61, v61
	v_cndmask_b32_e32 v61, 0, v61, vcc
	v_cndmask_b32_e64 v97, v61, v60, s[4:5]
	v_cvt_f16_f32_e32 v60, v48
	v_cvt_f32_f16_e32 v61, v60
	v_sub_f32_e32 v61, v48, v61
	v_cvt_f16_f32_e32 v61, v61
	v_cndmask_b32_e32 v61, 0, v61, vcc
	v_cndmask_b32_e64 v98, v61, v60, s[4:5]
	v_cvt_f16_f32_e32 v60, v49
	v_cvt_f32_f16_e32 v61, v60
	v_sub_f32_e32 v61, v49, v61
	v_cvt_f16_f32_e32 v61, v61
	v_cndmask_b32_e32 v61, 0, v61, vcc
	v_cndmask_b32_e64 v99, v61, v60, s[4:5]
	v_cvt_f16_f32_e32 v60, v50
	v_cvt_f32_f16_e32 v61, v60
	v_sub_f32_e32 v61, v50, v61
	v_cvt_f16_f32_e32 v61, v61
	v_cndmask_b32_e32 v61, 0, v61, vcc
	v_cndmask_b32_e64 v100, v61, v60, s[4:5]
	v_cvt_f16_f32_e32 v60, v51
	v_cvt_f32_f16_e32 v61, v60
	v_sub_f32_e32 v61, v51, v61
	v_cvt_f16_f32_e32 v61, v61
	v_cndmask_b32_e32 v61, 0, v61, vcc
	v_cndmask_b32_e64 v101, v61, v60, s[4:5]
	v_cvt_f16_f32_e32 v60, v52
	v_cvt_f32_f16_e32 v61, v60
	v_sub_f32_e32 v61, v52, v61
	v_cvt_f16_f32_e32 v61, v61
	v_cndmask_b32_e32 v61, 0, v61, vcc
	v_cndmask_b32_e64 v102, v61, v60, s[4:5]
	v_cvt_f16_f32_e32 v60, v53
	v_cvt_f32_f16_e32 v61, v60
	v_sub_f32_e32 v61, v53, v61
	v_cvt_f16_f32_e32 v61, v61
	v_cndmask_b32_e32 v61, 0, v61, vcc
	v_cndmask_b32_e64 v103, v61, v60, s[4:5]
	v_cvt_f16_f32_e32 v60, v54
	v_cvt_f32_f16_e32 v61, v60
	v_sub_f32_e32 v61, v54, v61
	v_cvt_f16_f32_e32 v61, v61
	v_cndmask_b32_e32 v61, 0, v61, vcc
	v_cndmask_b32_e64 v104, v61, v60, s[4:5]
	v_cvt_f16_f32_e32 v60, v55
	v_cvt_f32_f16_e32 v61, v60
	v_sub_f32_e32 v61, v55, v61
	v_cvt_f16_f32_e32 v61, v61
	v_cndmask_b32_e32 v61, 0, v61, vcc
	v_cndmask_b32_e64 v105, v61, v60, s[4:5]
	v_cvt_f16_f32_e32 v60, v56
	v_cvt_f32_f16_e32 v61, v60
	v_sub_f32_e32 v61, v56, v61
	v_cvt_f16_f32_e32 v61, v61
	v_cndmask_b32_e32 v61, 0, v61, vcc
	v_cndmask_b32_e64 v106, v61, v60, s[4:5]
	v_cvt_f16_f32_e32 v60, v57
	v_cvt_f32_f16_e32 v61, v60
	v_sub_f32_e32 v61, v57, v61
	v_cvt_f16_f32_e32 v61, v61
	v_cndmask_b32_e32 v61, 0, v61, vcc
	v_cndmask_b32_e64 v107, v61, v60, s[4:5]
	v_cvt_f16_f32_e32 v60, v58
	v_cvt_f32_f16_e32 v61, v60
	v_sub_f32_e32 v61, v58, v61
	v_cvt_f16_f32_e32 v61, v61
	v_cndmask_b32_e32 v61, 0, v61, vcc
	v_cndmask_b32_e64 v108, v61, v60, s[4:5]
	v_cvt_f16_f32_e32 v60, v59
	v_cvt_f32_f16_e32 v61, v60
	v_sub_f32_e32 v61, v59, v61
	v_cvt_f16_f32_e32 v61, v61
	v_cndmask_b32_e32 v61, 0, v61, vcc
	v_cndmask_b32_e64 v109, v61, v60, s[4:5]
	v_pack_b32_f16 v116, v94, v95
	v_pack_b32_f16 v117, v96, v97
	v_pack_b32_f16 v118, v98, v99
	v_pack_b32_f16 v119, v100, v101
	v_pack_b32_f16 v120, v102, v103
	v_pack_b32_f16 v121, v104, v105
	v_pack_b32_f16 v122, v106, v107
	v_pack_b32_f16 v123, v108, v109
	s_cmp_eq_u32 s34, 0
	s_cbranch_scc1 .Lcb_r0
	s_cmp_eq_u32 s34, 1
	s_cbranch_scc1 .Lcb_r1
	s_cmp_eq_u32 s34, 2
	s_cbranch_scc1 .Lcb_r2
	s_barrier
	ds_read_b128 v[44:47], v75 offset:0
	ds_read_b128 v[68:71], v75 offset:1024
	s_waitcnt lgkmcnt(0)
	v_mfma_f32_16x16x32_f16 v[84:87], v[2:5], v[44:47], v[18:21]
	v_mfma_f32_16x16x32_f16 v[88:91], v[14:17], v[44:47], v[38:41]
	v_mfma_f32_16x16x32_f16 v[84:87], v[6:9], v[68:71], v[84:87]
	v_mfma_f32_16x16x32_f16 v[88:91], v[10:13], v[68:71], v[88:91]
	s_barrier
	ds_read_b128 v[56:59], v75 offset:6144
	ds_read_b128 v[60:63], v75 offset:7168
	s_waitcnt lgkmcnt(1)
	v_mfma_f32_16x16x32_f16 v[84:87], v[30:33], v[56:59], v[84:87]
	v_mfma_f32_16x16x32_f16 v[88:91], v[22:25], v[56:59], v[88:91]
	s_waitcnt lgkmcnt(0)
	v_mfma_f32_16x16x32_f16 v[84:87], v[34:37], v[60:63], v[84:87]
	v_mfma_f32_16x16x32_f16 v[88:91], v[26:29], v[60:63], v[88:91]
	ds_read_b128 v[44:47], v75 offset:2048
	ds_read_b128 v[68:71], v75 offset:3072
	s_nop 5
	v_exp_f32_e32 v94, v86
	v_exp_f32_e32 v95, v90
	v_exp_f32_e32 v96, v84
	v_exp_f32_e32 v97, v88
	v_exp_f32_e32 v98, v85
	v_exp_f32_e32 v99, v89
	v_pk_add_f32 v[100:101], v[94:95], 1.0 op_sel_hi:[1,0]
	v_pk_fma_f32 v[102:103], v[94:95], s[8:9], v[92:93] op_sel_hi:[1,0,0]
	v_pk_fma_f32 v[100:101], v[96:97], v[100:101], v[100:101]
	v_pk_fma_f32 v[104:105], v[100:101], v[98:99], v[100:101]
	v_rcp_f32_e32 v104, v104
	v_rcp_f32_e32 v105, v105
	v_pk_fma_f32 v[102:103], v[102:103], v[98:99], v[102:103]
	v_pk_fma_f32 v[102:103], v[64:65], v[100:101], v[102:103]
	v_exp_f32_e32 v106, v87
	v_pk_mul_f32 v[64:65], v[102:103], v[104:105]
	v_exp_f32_e32 v108, v64
	v_exp_f32_e32 v109, v65
	v_exp_f32_e32 v107, v91
	v_pk_add_f32 v[110:111], v[108:109], 1.0 op_sel_hi:[1,0]
	v_pk_fma_f32 v[110:111], v[110:111], v[106:107], v[110:111]
	v_rcp_f32_e32 v110, v110
	v_rcp_f32_e32 v111, v111
	v_pk_add_f32 v[112:113], v[108:109], -1.0 op_sel_hi:[1,0]
	v_pk_mul_f32 v[112:113], v[112:113], v[110:111]
	v_cvt_pk_f16_f32 v114, v112, v113
	ds_write_b32 v81, v114 offset:4096
	s_waitcnt lgkmcnt(1)
	v_mfma_f32_16x16x32_f16 v[84:87], v[2:5], v[44:47], v[18:21]
	v_mfma_f32_16x16x32_f16 v[88:91], v[14:17], v[44:47], v[38:41]
	v_mfma_f32_16x16x32_f16 v[84:87], v[6:9], v[68:71], v[84:87]
	v_mfma_f32_16x16x32_f16 v[88:91], v[10:13], v[68:71], v[88:91]
	s_waitcnt lgkmcnt(0)
	s_barrier
	ds_read_b128 v[56:59], v75 offset:4096
	ds_read_b128 v[60:63], v75 offset:5120
	s_waitcnt lgkmcnt(1)
	v_mfma_f32_16x16x32_f16 v[84:87], v[30:33], v[56:59], v[84:87]
	v_mfma_f32_16x16x32_f16 v[88:91], v[22:25], v[56:59], v[88:91]
	s_waitcnt lgkmcnt(0)
	v_mfma_f32_16x16x32_f16 v[84:87], v[34:37], v[60:63], v[84:87]
	v_mfma_f32_16x16x32_f16 v[88:91], v[26:29], v[60:63], v[88:91]
	ds_read_b128 v[44:47], v75 offset:0
	ds_read_b128 v[68:71], v75 offset:1024
	s_nop 5
	v_exp_f32_e32 v94, v86
	v_exp_f32_e32 v95, v90
	v_exp_f32_e32 v96, v84
	v_exp_f32_e32 v97, v88
	v_exp_f32_e32 v98, v85
	v_exp_f32_e32 v99, v89
	v_pk_add_f32 v[100:101], v[94:95], 1.0 op_sel_hi:[1,0]
	v_pk_fma_f32 v[102:103], v[94:95], s[8:9], v[92:93] op_sel_hi:[1,0,0]
	v_pk_fma_f32 v[100:101], v[96:97], v[100:101], v[100:101]
	v_pk_fma_f32 v[104:105], v[100:101], v[98:99], v[100:101]
	v_rcp_f32_e32 v104, v104
	v_rcp_f32_e32 v105, v105
	v_pk_fma_f32 v[102:103], v[102:103], v[98:99], v[102:103]
	v_pk_fma_f32 v[102:103], v[64:65], v[100:101], v[102:103]
	v_exp_f32_e32 v106, v87
	v_pk_mul_f32 v[64:65], v[102:103], v[104:105]
	v_exp_f32_e32 v108, v64
	v_exp_f32_e32 v109, v65
	v_exp_f32_e32 v107, v91
	v_pk_add_f32 v[110:111], v[108:109], 1.0 op_sel_hi:[1,0]
	v_pk_fma_f32 v[110:111], v[110:111], v[106:107], v[110:111]
	v_rcp_f32_e32 v110, v110
	v_rcp_f32_e32 v111, v111
	v_pk_add_f32 v[112:113], v[108:109], -1.0 op_sel_hi:[1,0]
	v_pk_mul_f32 v[112:113], v[112:113], v[110:111]
	v_cvt_pk_f16_f32 v114, v112, v113
	ds_write_b32 v81, v114 offset:6144
	s_waitcnt lgkmcnt(1)
	v_mfma_f32_16x16x32_f16 v[84:87], v[2:5], v[44:47], v[18:21]
	v_mfma_f32_16x16x32_f16 v[88:91], v[14:17], v[44:47], v[38:41]
	v_mfma_f32_16x16x32_f16 v[84:87], v[6:9], v[68:71], v[84:87]
	v_mfma_f32_16x16x32_f16 v[88:91], v[10:13], v[68:71], v[88:91]
	s_waitcnt lgkmcnt(0)
	.p2align	6
.Lcb3_loop:
	s_barrier
	ds_read_b128 v[56:59], v75 offset:6144
	ds_read_b128 v[60:63], v75 offset:7168
	s_waitcnt lgkmcnt(1)
	v_mfma_f32_16x16x32_f16 v[84:87], v[30:33], v[56:59], v[84:87]
	v_mfma_f32_16x16x32_f16 v[88:91], v[22:25], v[56:59], v[88:91]
	s_waitcnt lgkmcnt(0)
	v_mfma_f32_16x16x32_f16 v[84:87], v[34:37], v[60:63], v[84:87]
	v_mfma_f32_16x16x32_f16 v[88:91], v[26:29], v[60:63], v[88:91]
	ds_read_b128 v[44:47], v75 offset:2048
	ds_read_b128 v[68:71], v75 offset:3072
	s_nop 5
	v_exp_f32_e32 v94, v86
	v_exp_f32_e32 v95, v90
	v_exp_f32_e32 v96, v84
	v_exp_f32_e32 v97, v88
	v_exp_f32_e32 v98, v85
	v_exp_f32_e32 v99, v89
	v_pk_add_f32 v[100:101], v[94:95], 1.0 op_sel_hi:[1,0]
	v_pk_fma_f32 v[102:103], v[94:95], s[8:9], v[92:93] op_sel_hi:[1,0,0]
	v_pk_fma_f32 v[100:101], v[96:97], v[100:101], v[100:101]
	v_pk_fma_f32 v[104:105], v[100:101], v[98:99], v[100:101]
	v_rcp_f32_e32 v104, v104
	v_rcp_f32_e32 v105, v105
	v_pk_fma_f32 v[102:103], v[102:103], v[98:99], v[102:103]
	v_pk_fma_f32 v[102:103], v[64:65], v[100:101], v[102:103]
	v_exp_f32_e32 v106, v87
	v_pk_mul_f32 v[64:65], v[102:103], v[104:105]
	v_exp_f32_e32 v108, v64
	v_exp_f32_e32 v109, v65
	v_exp_f32_e32 v107, v91
	v_pk_add_f32 v[110:111], v[108:109], 1.0 op_sel_hi:[1,0]
	v_pk_fma_f32 v[110:111], v[110:111], v[106:107], v[110:111]
	v_rcp_f32_e32 v110, v110
	v_rcp_f32_e32 v111, v111
	v_pk_add_f32 v[112:113], v[108:109], -1.0 op_sel_hi:[1,0]
	v_pk_mul_f32 v[112:113], v[112:113], v[110:111]
	v_cvt_pk_f16_f32 v114, v112, v113
	ds_write_b32 v81, v114 offset:4096
	s_waitcnt lgkmcnt(1)
	v_mfma_f32_16x16x32_f16 v[84:87], v[2:5], v[44:47], v[18:21]
	v_mfma_f32_16x16x32_f16 v[88:91], v[14:17], v[44:47], v[38:41]
	v_mfma_f32_16x16x32_f16 v[84:87], v[6:9], v[68:71], v[84:87]
	v_mfma_f32_16x16x32_f16 v[88:91], v[10:13], v[68:71], v[88:91]
	s_waitcnt lgkmcnt(0)
	s_barrier
	ds_read_b128 v[56:59], v75 offset:4096
	ds_read_b128 v[60:63], v75 offset:5120
	s_waitcnt lgkmcnt(1)
	v_mfma_f32_16x16x32_f16 v[84:87], v[30:33], v[56:59], v[84:87]
	v_mfma_f32_16x16x32_f16 v[88:91], v[22:25], v[56:59], v[88:91]
	s_waitcnt lgkmcnt(0)
	v_mfma_f32_16x16x32_f16 v[84:87], v[34:37], v[60:63], v[84:87]
	v_mfma_f32_16x16x32_f16 v[88:91], v[26:29], v[60:63], v[88:91]
	ds_read_b128 v[44:47], v75 offset:0
	ds_read_b128 v[68:71], v75 offset:1024
	s_nop 5
	v_exp_f32_e32 v94, v86
	v_exp_f32_e32 v95, v90
	v_exp_f32_e32 v96, v84
	v_exp_f32_e32 v97, v88
	v_exp_f32_e32 v98, v85
	v_exp_f32_e32 v99, v89
	v_pk_add_f32 v[100:101], v[94:95], 1.0 op_sel_hi:[1,0]
	v_pk_fma_f32 v[102:103], v[94:95], s[8:9], v[92:93] op_sel_hi:[1,0,0]
	v_pk_fma_f32 v[100:101], v[96:97], v[100:101], v[100:101]
	v_pk_fma_f32 v[104:105], v[100:101], v[98:99], v[100:101]
	v_rcp_f32_e32 v104, v104
	v_rcp_f32_e32 v105, v105
	v_pk_fma_f32 v[102:103], v[102:103], v[98:99], v[102:103]
	v_pk_fma_f32 v[102:103], v[64:65], v[100:101], v[102:103]
	v_exp_f32_e32 v106, v87
	v_pk_mul_f32 v[64:65], v[102:103], v[104:105]
	v_exp_f32_e32 v108, v64
	v_exp_f32_e32 v109, v65
	v_exp_f32_e32 v107, v91
	v_pk_add_f32 v[110:111], v[108:109], 1.0 op_sel_hi:[1,0]
	v_pk_fma_f32 v[110:111], v[110:111], v[106:107], v[110:111]
	v_rcp_f32_e32 v110, v110
	v_rcp_f32_e32 v111, v111
	v_pk_add_f32 v[112:113], v[108:109], -1.0 op_sel_hi:[1,0]
	v_pk_mul_f32 v[112:113], v[112:113], v[110:111]
	v_cvt_pk_f16_f32 v114, v112, v113
	ds_write_b32 v81, v114 offset:6144
	s_waitcnt lgkmcnt(1)
	v_mfma_f32_16x16x32_f16 v[84:87], v[2:5], v[44:47], v[18:21]
	v_mfma_f32_16x16x32_f16 v[88:91], v[14:17], v[44:47], v[38:41]
	v_mfma_f32_16x16x32_f16 v[84:87], v[6:9], v[68:71], v[84:87]
	v_mfma_f32_16x16x32_f16 v[88:91], v[10:13], v[68:71], v[88:91]
	s_waitcnt lgkmcnt(0)
	s_barrier
	ds_read_b128 v[56:59], v75 offset:6144
	ds_read_b128 v[60:63], v75 offset:7168
	s_waitcnt lgkmcnt(1)
	v_mfma_f32_16x16x32_f16 v[84:87], v[30:33], v[56:59], v[84:87]
	v_mfma_f32_16x16x32_f16 v[88:91], v[22:25], v[56:59], v[88:91]
	s_waitcnt lgkmcnt(0)
	v_mfma_f32_16x16x32_f16 v[84:87], v[34:37], v[60:63], v[84:87]
	v_mfma_f32_16x16x32_f16 v[88:91], v[26:29], v[60:63], v[88:91]
	ds_read_b128 v[44:47], v75 offset:2048
	ds_read_b128 v[68:71], v75 offset:3072
	s_nop 5
	v_exp_f32_e32 v94, v86
	v_exp_f32_e32 v95, v90
	v_exp_f32_e32 v96, v84
	v_exp_f32_e32 v97, v88
	v_exp_f32_e32 v98, v85
	v_exp_f32_e32 v99, v89
	v_pk_add_f32 v[100:101], v[94:95], 1.0 op_sel_hi:[1,0]
	v_pk_fma_f32 v[102:103], v[94:95], s[8:9], v[92:93] op_sel_hi:[1,0,0]
	v_pk_fma_f32 v[100:101], v[96:97], v[100:101], v[100:101]
	v_pk_fma_f32 v[104:105], v[100:101], v[98:99], v[100:101]
	v_rcp_f32_e32 v104, v104
	v_rcp_f32_e32 v105, v105
	v_pk_fma_f32 v[102:103], v[102:103], v[98:99], v[102:103]
	v_pk_fma_f32 v[102:103], v[64:65], v[100:101], v[102:103]
	v_exp_f32_e32 v106, v87
	v_pk_mul_f32 v[64:65], v[102:103], v[104:105]
	v_exp_f32_e32 v108, v64
	v_exp_f32_e32 v109, v65
	v_exp_f32_e32 v107, v91
	v_pk_add_f32 v[110:111], v[108:109], 1.0 op_sel_hi:[1,0]
	v_pk_fma_f32 v[110:111], v[110:111], v[106:107], v[110:111]
	v_rcp_f32_e32 v110, v110
	v_rcp_f32_e32 v111, v111
	v_pk_add_f32 v[112:113], v[108:109], -1.0 op_sel_hi:[1,0]
	v_pk_mul_f32 v[112:113], v[112:113], v[110:111]
	v_cvt_pk_f16_f32 v114, v112, v113
	ds_write_b32 v81, v114 offset:4096
	s_waitcnt lgkmcnt(1)
	v_mfma_f32_16x16x32_f16 v[84:87], v[2:5], v[44:47], v[18:21]
	v_mfma_f32_16x16x32_f16 v[88:91], v[14:17], v[44:47], v[38:41]
	v_mfma_f32_16x16x32_f16 v[84:87], v[6:9], v[68:71], v[84:87]
	v_mfma_f32_16x16x32_f16 v[88:91], v[10:13], v[68:71], v[88:91]
	s_waitcnt lgkmcnt(0)
	s_barrier
	ds_read_b128 v[56:59], v75 offset:4096
	ds_read_b128 v[60:63], v75 offset:5120
	s_waitcnt lgkmcnt(1)
	v_mfma_f32_16x16x32_f16 v[84:87], v[30:33], v[56:59], v[84:87]
	v_mfma_f32_16x16x32_f16 v[88:91], v[22:25], v[56:59], v[88:91]
	s_waitcnt lgkmcnt(0)
	v_mfma_f32_16x16x32_f16 v[84:87], v[34:37], v[60:63], v[84:87]
	v_mfma_f32_16x16x32_f16 v[88:91], v[26:29], v[60:63], v[88:91]
	ds_read_b128 v[44:47], v75 offset:0
	ds_read_b128 v[68:71], v75 offset:1024
	s_nop 5
	v_exp_f32_e32 v94, v86
	v_exp_f32_e32 v95, v90
	v_exp_f32_e32 v96, v84
	v_exp_f32_e32 v97, v88
	v_exp_f32_e32 v98, v85
	v_exp_f32_e32 v99, v89
	v_pk_add_f32 v[100:101], v[94:95], 1.0 op_sel_hi:[1,0]
	v_pk_fma_f32 v[102:103], v[94:95], s[8:9], v[92:93] op_sel_hi:[1,0,0]
	v_pk_fma_f32 v[100:101], v[96:97], v[100:101], v[100:101]
	v_pk_fma_f32 v[104:105], v[100:101], v[98:99], v[100:101]
	v_rcp_f32_e32 v104, v104
	v_rcp_f32_e32 v105, v105
	v_pk_fma_f32 v[102:103], v[102:103], v[98:99], v[102:103]
	v_pk_fma_f32 v[102:103], v[64:65], v[100:101], v[102:103]
	v_exp_f32_e32 v106, v87
	v_pk_mul_f32 v[64:65], v[102:103], v[104:105]
	v_exp_f32_e32 v108, v64
	v_exp_f32_e32 v109, v65
	v_exp_f32_e32 v107, v91
	v_pk_add_f32 v[110:111], v[108:109], 1.0 op_sel_hi:[1,0]
	v_pk_fma_f32 v[110:111], v[110:111], v[106:107], v[110:111]
	v_rcp_f32_e32 v110, v110
	v_rcp_f32_e32 v111, v111
	v_pk_add_f32 v[112:113], v[108:109], -1.0 op_sel_hi:[1,0]
	v_pk_mul_f32 v[112:113], v[112:113], v[110:111]
	v_cvt_pk_f16_f32 v114, v112, v113
	ds_write_b32 v81, v114 offset:6144
	s_waitcnt lgkmcnt(1)
	v_mfma_f32_16x16x32_f16 v[84:87], v[2:5], v[44:47], v[18:21]
	v_mfma_f32_16x16x32_f16 v[88:91], v[14:17], v[44:47], v[38:41]
	v_mfma_f32_16x16x32_f16 v[84:87], v[6:9], v[68:71], v[84:87]
	v_mfma_f32_16x16x32_f16 v[88:91], v[10:13], v[68:71], v[88:91]
	s_waitcnt lgkmcnt(0)
	v_min_f32_e32 v64, 0x42700000, v64
	v_min_f32_e32 v65, 0x42700000, v65
	s_add_u32 s12, s12, 4
	v_add_u32_e32 v124, 16, v124
	s_cmp_lt_u32 s12, 452
	s_cbranch_scc1 .Lcb3_loop
	s_barrier
	ds_read_b128 v[56:59], v75 offset:6144
	ds_read_b128 v[60:63], v75 offset:7168
	s_waitcnt lgkmcnt(0)
	s_waitcnt lgkmcnt(0)
	s_barrier
	s_waitcnt lgkmcnt(0)
	s_endpgm
.Lcb_r0:
	s_barrier
	ds_read_b128 v[44:47], v75 offset:0
	ds_read_b128 v[68:71], v75 offset:1024
	s_waitcnt lgkmcnt(0)
	v_mfma_f32_16x16x32_f16 v[84:87], v[2:5], v[44:47], v[18:21]
	v_mfma_f32_16x16x32_f16 v[88:91], v[14:17], v[44:47], v[38:41]
	v_mfma_f32_16x16x32_f16 v[84:87], v[6:9], v[68:71], v[84:87]
	v_mfma_f32_16x16x32_f16 v[88:91], v[10:13], v[68:71], v[88:91]
	s_barrier
	ds_read_b128 v[56:59], v75 offset:6144
	ds_read_b128 v[60:63], v75 offset:7168
	s_waitcnt lgkmcnt(1)
	v_mfma_f32_16x16x32_f16 v[84:87], v[30:33], v[56:59], v[84:87]
	v_mfma_f32_16x16x32_f16 v[88:91], v[22:25], v[56:59], v[88:91]
	s_waitcnt lgkmcnt(0)
	v_mfma_f32_16x16x32_f16 v[84:87], v[34:37], v[60:63], v[84:87]
	v_mfma_f32_16x16x32_f16 v[88:91], v[26:29], v[60:63], v[88:91]
	ds_read_b128 v[44:47], v75 offset:2048
	ds_read_b128 v[68:71], v75 offset:3072
	s_nop 5
	v_exp_f32_e32 v94, v86
	v_exp_f32_e32 v95, v90
	v_exp_f32_e32 v96, v84
	v_exp_f32_e32 v97, v88
	v_exp_f32_e32 v98, v85
	v_exp_f32_e32 v99, v89
	v_pk_add_f32 v[100:101], v[94:95], 1.0 op_sel_hi:[1,0]
	v_pk_fma_f32 v[102:103], v[94:95], s[8:9], v[92:93] op_sel_hi:[1,0,0]
	v_pk_fma_f32 v[100:101], v[96:97], v[100:101], v[100:101]
	v_pk_fma_f32 v[104:105], v[100:101], v[98:99], v[100:101]
	v_rcp_f32_e32 v104, v104
	v_rcp_f32_e32 v105, v105
	v_pk_fma_f32 v[102:103], v[102:103], v[98:99], v[102:103]
	v_pk_fma_f32 v[102:103], v[64:65], v[100:101], v[102:103]
	v_exp_f32_e32 v106, v87
	v_pk_mul_f32 v[64:65], v[102:103], v[104:105]
	v_exp_f32_e32 v108, v64
	v_exp_f32_e32 v109, v65
	v_exp_f32_e32 v107, v91
	v_pk_add_f32 v[110:111], v[108:109], 1.0 op_sel_hi:[1,0]
	v_pk_fma_f32 v[110:111], v[110:111], v[106:107], v[110:111]
	v_rcp_f32_e32 v110, v110
	v_rcp_f32_e32 v111, v111
	v_pk_add_f32 v[112:113], v[108:109], -1.0 op_sel_hi:[1,0]
	v_pk_mul_f32 v[112:113], v[112:113], v[110:111]
	v_cvt_pk_f16_f32 v114, v112, v113
	ds_write_b32 v81, v114 offset:4096
	s_waitcnt lgkmcnt(1)
	v_mfma_f32_16x16x32_f16 v[84:87], v[2:5], v[44:47], v[18:21]
	v_mfma_f32_16x16x32_f16 v[88:91], v[14:17], v[44:47], v[38:41]
	v_mfma_f32_16x16x32_f16 v[84:87], v[6:9], v[68:71], v[84:87]
	v_mfma_f32_16x16x32_f16 v[88:91], v[10:13], v[68:71], v[88:91]
	s_waitcnt lgkmcnt(0)
	s_barrier
	ds_read_b128 v[56:59], v75 offset:4096
	ds_read_b128 v[60:63], v75 offset:5120
	s_waitcnt lgkmcnt(1)
	v_mfma_f32_16x16x32_f16 v[84:87], v[30:33], v[56:59], v[84:87]
	v_mfma_f32_16x16x32_f16 v[88:91], v[22:25], v[56:59], v[88:91]
	s_waitcnt lgkmcnt(0)
	v_mfma_f32_16x16x32_f16 v[84:87], v[34:37], v[60:63], v[84:87]
	v_mfma_f32_16x16x32_f16 v[88:91], v[26:29], v[60:63], v[88:91]
	ds_read_b128 v[44:47], v75 offset:0
	ds_read_b128 v[68:71], v75 offset:1024
	v_mfma_f32_16x16x32_f16 v[50:53], v[116:119], v[56:59], 0
	s_nop 5
	v_exp_f32_e32 v94, v86
	v_exp_f32_e32 v95, v90
	v_exp_f32_e32 v96, v84
	v_exp_f32_e32 v97, v88
	v_exp_f32_e32 v98, v85
	v_exp_f32_e32 v99, v89
	v_add_f32_e32 v125, v50, v51
	v_add_f32_e32 v125, s28, v125
	s_mov_b64 s[16:17], exec
	s_mov_b64 exec, s[30:31]
	ds_write_b32 v74, v125 offset:128
	s_mov_b64 exec, s[16:17]
	v_pk_add_f32 v[100:101], v[94:95], 1.0 op_sel_hi:[1,0]
	v_pk_fma_f32 v[102:103], v[94:95], s[8:9], v[92:93] op_sel_hi:[1,0,0]
	v_pk_fma_f32 v[100:101], v[96:97], v[100:101], v[100:101]
	v_pk_fma_f32 v[104:105], v[100:101], v[98:99], v[100:101]
	v_rcp_f32_e32 v104, v104
	v_rcp_f32_e32 v105, v105
	v_pk_fma_f32 v[102:103], v[102:103], v[98:99], v[102:103]
	v_pk_fma_f32 v[102:103], v[64:65], v[100:101], v[102:103]
	v_exp_f32_e32 v106, v87
	v_pk_mul_f32 v[64:65], v[102:103], v[104:105]
	v_exp_f32_e32 v108, v64
	v_exp_f32_e32 v109, v65
	v_exp_f32_e32 v107, v91
	v_pk_add_f32 v[110:111], v[108:109], 1.0 op_sel_hi:[1,0]
	v_pk_fma_f32 v[110:111], v[110:111], v[106:107], v[110:111]
	v_rcp_f32_e32 v110, v110
	v_rcp_f32_e32 v111, v111
	v_pk_add_f32 v[112:113], v[108:109], -1.0 op_sel_hi:[1,0]
	v_pk_mul_f32 v[112:113], v[112:113], v[110:111]
	v_cvt_pk_f16_f32 v114, v112, v113
	ds_write_b32 v81, v114 offset:6144
	s_waitcnt lgkmcnt(1)
	v_mfma_f32_16x16x32_f16 v[84:87], v[2:5], v[44:47], v[18:21]
	v_mfma_f32_16x16x32_f16 v[88:91], v[14:17], v[44:47], v[38:41]
	v_mfma_f32_16x16x32_f16 v[84:87], v[6:9], v[68:71], v[84:87]
	v_mfma_f32_16x16x32_f16 v[88:91], v[10:13], v[68:71], v[88:91]
	s_waitcnt lgkmcnt(0)
	.p2align	6
.Lcb0_loop:
	s_barrier
	ds_read_b128 v[56:59], v75 offset:6144
	ds_read_b128 v[60:63], v75 offset:7168
	s_waitcnt lgkmcnt(1)
	v_mfma_f32_16x16x32_f16 v[84:87], v[30:33], v[56:59], v[84:87]
	v_mfma_f32_16x16x32_f16 v[88:91], v[22:25], v[56:59], v[88:91]
	s_waitcnt lgkmcnt(0)
	v_mfma_f32_16x16x32_f16 v[84:87], v[34:37], v[60:63], v[84:87]
	v_mfma_f32_16x16x32_f16 v[88:91], v[26:29], v[60:63], v[88:91]
	ds_read_b128 v[44:47], v75 offset:2048
	ds_read_b128 v[68:71], v75 offset:3072
	v_mfma_f32_16x16x32_f16 v[50:53], v[116:119], v[56:59], 0
	s_nop 5
	v_exp_f32_e32 v94, v86
	v_exp_f32_e32 v95, v90
	v_exp_f32_e32 v96, v84
	v_exp_f32_e32 v97, v88
	v_exp_f32_e32 v98, v85
	v_exp_f32_e32 v99, v89
	v_add_f32_e32 v125, v50, v51
	v_add_f32_e32 v125, s28, v125
	s_mov_b64 s[16:17], exec
	s_mov_b64 exec, s[30:31]
	ds_write_b32 v74, v125 offset:0
	s_mov_b64 exec, s[16:17]
	v_pk_add_f32 v[100:101], v[94:95], 1.0 op_sel_hi:[1,0]
	v_pk_fma_f32 v[102:103], v[94:95], s[8:9], v[92:93] op_sel_hi:[1,0,0]
	v_pk_fma_f32 v[100:101], v[96:97], v[100:101], v[100:101]
	v_pk_fma_f32 v[104:105], v[100:101], v[98:99], v[100:101]
	v_rcp_f32_e32 v104, v104
	v_rcp_f32_e32 v105, v105
	v_pk_fma_f32 v[102:103], v[102:103], v[98:99], v[102:103]
	v_pk_fma_f32 v[102:103], v[64:65], v[100:101], v[102:103]
	v_exp_f32_e32 v106, v87
	v_pk_mul_f32 v[64:65], v[102:103], v[104:105]
	v_exp_f32_e32 v108, v64
	v_exp_f32_e32 v109, v65
	v_exp_f32_e32 v107, v91
	v_pk_add_f32 v[110:111], v[108:109], 1.0 op_sel_hi:[1,0]
	v_pk_fma_f32 v[110:111], v[110:111], v[106:107], v[110:111]
	v_rcp_f32_e32 v110, v110
	v_rcp_f32_e32 v111, v111
	v_pk_add_f32 v[112:113], v[108:109], -1.0 op_sel_hi:[1,0]
	v_pk_mul_f32 v[112:113], v[112:113], v[110:111]
	v_cvt_pk_f16_f32 v114, v112, v113
	ds_write_b32 v81, v114 offset:4096
	s_waitcnt lgkmcnt(1)
	v_mfma_f32_16x16x32_f16 v[84:87], v[2:5], v[44:47], v[18:21]
	v_mfma_f32_16x16x32_f16 v[88:91], v[14:17], v[44:47], v[38:41]
	v_mfma_f32_16x16x32_f16 v[84:87], v[6:9], v[68:71], v[84:87]
	v_mfma_f32_16x16x32_f16 v[88:91], v[10:13], v[68:71], v[88:91]
	s_waitcnt lgkmcnt(0)
	s_barrier
	ds_read_b128 v[56:59], v75 offset:4096
	ds_read_b128 v[60:63], v75 offset:5120
	s_waitcnt lgkmcnt(1)
	v_mfma_f32_16x16x32_f16 v[84:87], v[30:33], v[56:59], v[84:87]
	v_mfma_f32_16x16x32_f16 v[88:91], v[22:25], v[56:59], v[88:91]
	s_waitcnt lgkmcnt(0)
	v_mfma_f32_16x16x32_f16 v[84:87], v[34:37], v[60:63], v[84:87]
	v_mfma_f32_16x16x32_f16 v[88:91], v[26:29], v[60:63], v[88:91]
	ds_read_b128 v[44:47], v75 offset:0
	ds_read_b128 v[68:71], v75 offset:1024
	v_mfma_f32_16x16x32_f16 v[50:53], v[116:119], v[56:59], 0
	s_nop 5
	v_exp_f32_e32 v94, v86
	v_exp_f32_e32 v95, v90
	v_exp_f32_e32 v96, v84
	v_exp_f32_e32 v97, v88
	v_exp_f32_e32 v98, v85
	v_exp_f32_e32 v99, v89
	v_add_f32_e32 v125, v50, v51
	v_add_f32_e32 v125, s28, v125
	s_mov_b64 s[16:17], exec
	s_mov_b64 exec, s[30:31]
	ds_write_b32 v74, v125 offset:128
	s_mov_b64 exec, s[16:17]
	v_pk_add_f32 v[100:101], v[94:95], 1.0 op_sel_hi:[1,0]
	v_pk_fma_f32 v[102:103], v[94:95], s[8:9], v[92:93] op_sel_hi:[1,0,0]
	v_pk_fma_f32 v[100:101], v[96:97], v[100:101], v[100:101]
	v_pk_fma_f32 v[104:105], v[100:101], v[98:99], v[100:101]
	v_rcp_f32_e32 v104, v104
	v_rcp_f32_e32 v105, v105
	v_pk_fma_f32 v[102:103], v[102:103], v[98:99], v[102:103]
	v_pk_fma_f32 v[102:103], v[64:65], v[100:101], v[102:103]
	v_exp_f32_e32 v106, v87
	v_pk_mul_f32 v[64:65], v[102:103], v[104:105]
	v_exp_f32_e32 v108, v64
	v_exp_f32_e32 v109, v65
	v_exp_f32_e32 v107, v91
	v_pk_add_f32 v[110:111], v[108:109], 1.0 op_sel_hi:[1,0]
	v_pk_fma_f32 v[110:111], v[110:111], v[106:107], v[110:111]
	v_rcp_f32_e32 v110, v110
	v_rcp_f32_e32 v111, v111
	v_pk_add_f32 v[112:113], v[108:109], -1.0 op_sel_hi:[1,0]
	v_pk_mul_f32 v[112:113], v[112:113], v[110:111]
	v_cvt_pk_f16_f32 v114, v112, v113
	ds_write_b32 v81, v114 offset:6144
	s_waitcnt lgkmcnt(1)
	v_mfma_f32_16x16x32_f16 v[84:87], v[2:5], v[44:47], v[18:21]
	v_mfma_f32_16x16x32_f16 v[88:91], v[14:17], v[44:47], v[38:41]
	v_mfma_f32_16x16x32_f16 v[84:87], v[6:9], v[68:71], v[84:87]
	v_mfma_f32_16x16x32_f16 v[88:91], v[10:13], v[68:71], v[88:91]
	s_waitcnt lgkmcnt(0)
	s_barrier
	ds_read_b128 v[56:59], v75 offset:6144
	ds_read_b128 v[60:63], v75 offset:7168
	s_waitcnt lgkmcnt(1)
	v_mfma_f32_16x16x32_f16 v[84:87], v[30:33], v[56:59], v[84:87]
	v_mfma_f32_16x16x32_f16 v[88:91], v[22:25], v[56:59], v[88:91]
	s_waitcnt lgkmcnt(0)
	v_mfma_f32_16x16x32_f16 v[84:87], v[34:37], v[60:63], v[84:87]
	v_mfma_f32_16x16x32_f16 v[88:91], v[26:29], v[60:63], v[88:91]
	ds_read_b128 v[44:47], v75 offset:2048
	ds_read_b128 v[68:71], v75 offset:3072
	v_mfma_f32_16x16x32_f16 v[50:53], v[116:119], v[56:59], 0
	s_nop 5
	v_exp_f32_e32 v94, v86
	v_exp_f32_e32 v95, v90
	v_exp_f32_e32 v96, v84
	v_exp_f32_e32 v97, v88
	v_exp_f32_e32 v98, v85
	v_exp_f32_e32 v99, v89
	v_add_f32_e32 v125, v50, v51
	v_add_f32_e32 v125, s28, v125
	s_mov_b64 s[16:17], exec
	s_mov_b64 exec, s[30:31]
	ds_write_b32 v74, v125 offset:0
	s_mov_b64 exec, s[16:17]
	v_pk_add_f32 v[100:101], v[94:95], 1.0 op_sel_hi:[1,0]
	v_pk_fma_f32 v[102:103], v[94:95], s[8:9], v[92:93] op_sel_hi:[1,0,0]
	v_pk_fma_f32 v[100:101], v[96:97], v[100:101], v[100:101]
	v_pk_fma_f32 v[104:105], v[100:101], v[98:99], v[100:101]
	v_rcp_f32_e32 v104, v104
	v_rcp_f32_e32 v105, v105
	v_pk_fma_f32 v[102:103], v[102:103], v[98:99], v[102:103]
	v_pk_fma_f32 v[102:103], v[64:65], v[100:101], v[102:103]
	v_exp_f32_e32 v106, v87
	v_pk_mul_f32 v[64:65], v[102:103], v[104:105]
	v_exp_f32_e32 v108, v64
	v_exp_f32_e32 v109, v65
	v_exp_f32_e32 v107, v91
	v_pk_add_f32 v[110:111], v[108:109], 1.0 op_sel_hi:[1,0]
	v_pk_fma_f32 v[110:111], v[110:111], v[106:107], v[110:111]
	v_rcp_f32_e32 v110, v110
	v_rcp_f32_e32 v111, v111
	v_pk_add_f32 v[112:113], v[108:109], -1.0 op_sel_hi:[1,0]
	v_pk_mul_f32 v[112:113], v[112:113], v[110:111]
	v_cvt_pk_f16_f32 v114, v112, v113
	ds_write_b32 v81, v114 offset:4096
	s_waitcnt lgkmcnt(1)
	v_mfma_f32_16x16x32_f16 v[84:87], v[2:5], v[44:47], v[18:21]
	v_mfma_f32_16x16x32_f16 v[88:91], v[14:17], v[44:47], v[38:41]
	v_mfma_f32_16x16x32_f16 v[84:87], v[6:9], v[68:71], v[84:87]
	v_mfma_f32_16x16x32_f16 v[88:91], v[10:13], v[68:71], v[88:91]
	s_waitcnt lgkmcnt(0)
	s_barrier
	ds_read_b128 v[56:59], v75 offset:4096
	ds_read_b128 v[60:63], v75 offset:5120
	s_waitcnt lgkmcnt(1)
	v_mfma_f32_16x16x32_f16 v[84:87], v[30:33], v[56:59], v[84:87]
	v_mfma_f32_16x16x32_f16 v[88:91], v[22:25], v[56:59], v[88:91]
	s_waitcnt lgkmcnt(0)
	v_mfma_f32_16x16x32_f16 v[84:87], v[34:37], v[60:63], v[84:87]
	v_mfma_f32_16x16x32_f16 v[88:91], v[26:29], v[60:63], v[88:91]
	ds_read_b128 v[44:47], v75 offset:0
	ds_read_b128 v[68:71], v75 offset:1024
	v_mfma_f32_16x16x32_f16 v[50:53], v[116:119], v[56:59], 0
	s_nop 5
	v_exp_f32_e32 v94, v86
	v_exp_f32_e32 v95, v90
	v_exp_f32_e32 v96, v84
	v_exp_f32_e32 v97, v88
	v_exp_f32_e32 v98, v85
	v_exp_f32_e32 v99, v89
	v_add_f32_e32 v125, v50, v51
	v_add_f32_e32 v125, s28, v125
	s_mov_b64 s[16:17], exec
	s_mov_b64 exec, s[30:31]
	ds_write_b32 v74, v125 offset:128
	s_mov_b64 exec, s[16:17]
	v_pk_add_f32 v[100:101], v[94:95], 1.0 op_sel_hi:[1,0]
	v_pk_fma_f32 v[102:103], v[94:95], s[8:9], v[92:93] op_sel_hi:[1,0,0]
	v_pk_fma_f32 v[100:101], v[96:97], v[100:101], v[100:101]
	v_pk_fma_f32 v[104:105], v[100:101], v[98:99], v[100:101]
	v_rcp_f32_e32 v104, v104
	v_rcp_f32_e32 v105, v105
	v_pk_fma_f32 v[102:103], v[102:103], v[98:99], v[102:103]
	v_pk_fma_f32 v[102:103], v[64:65], v[100:101], v[102:103]
	v_exp_f32_e32 v106, v87
	v_pk_mul_f32 v[64:65], v[102:103], v[104:105]
	v_exp_f32_e32 v108, v64
	v_exp_f32_e32 v109, v65
	v_exp_f32_e32 v107, v91
	v_pk_add_f32 v[110:111], v[108:109], 1.0 op_sel_hi:[1,0]
	v_pk_fma_f32 v[110:111], v[110:111], v[106:107], v[110:111]
	v_rcp_f32_e32 v110, v110
	v_rcp_f32_e32 v111, v111
	v_pk_add_f32 v[112:113], v[108:109], -1.0 op_sel_hi:[1,0]
	v_pk_mul_f32 v[112:113], v[112:113], v[110:111]
	v_cvt_pk_f16_f32 v114, v112, v113
	ds_write_b32 v81, v114 offset:6144
	s_waitcnt lgkmcnt(1)
	v_mfma_f32_16x16x32_f16 v[84:87], v[2:5], v[44:47], v[18:21]
	v_mfma_f32_16x16x32_f16 v[88:91], v[14:17], v[44:47], v[38:41]
	v_mfma_f32_16x16x32_f16 v[84:87], v[6:9], v[68:71], v[84:87]
	v_mfma_f32_16x16x32_f16 v[88:91], v[10:13], v[68:71], v[88:91]
	s_waitcnt lgkmcnt(0)
	v_min_f32_e32 v64, 0x42700000, v64
	v_min_f32_e32 v65, 0x42700000, v65
	s_add_u32 s12, s12, 4
	v_add_u32_e32 v124, 16, v124
	s_cmp_lt_u32 s12, 452
	s_cbranch_scc1 .Lcb0_loop
	s_barrier
	ds_read_b128 v[56:59], v75 offset:6144
	ds_read_b128 v[60:63], v75 offset:7168
	s_waitcnt lgkmcnt(0)
	v_mfma_f32_16x16x32_f16 v[50:53], v[116:119], v[56:59], 0
	s_nop 7
	v_add_f32_e32 v125, v50, v51
	v_add_f32_e32 v125, s28, v125
	s_mov_b64 s[16:17], exec
	s_mov_b64 exec, s[30:31]
	ds_write_b32 v74, v125 offset:0
	s_mov_b64 exec, s[16:17]
	s_waitcnt lgkmcnt(0)
	s_barrier
	s_waitcnt lgkmcnt(0)
	s_endpgm
.Lcb_r1:
	s_barrier
	ds_read_b128 v[44:47], v75 offset:0
	ds_read_b128 v[68:71], v75 offset:1024
	s_waitcnt lgkmcnt(0)
	v_mfma_f32_16x16x32_f16 v[84:87], v[2:5], v[44:47], v[18:21]
	v_mfma_f32_16x16x32_f16 v[88:91], v[14:17], v[44:47], v[38:41]
	v_mfma_f32_16x16x32_f16 v[84:87], v[6:9], v[68:71], v[84:87]
	v_mfma_f32_16x16x32_f16 v[88:91], v[10:13], v[68:71], v[88:91]
	s_barrier
	ds_read_b128 v[56:59], v75 offset:6144
	ds_read_b128 v[60:63], v75 offset:7168
	s_waitcnt lgkmcnt(1)
	v_mfma_f32_16x16x32_f16 v[84:87], v[30:33], v[56:59], v[84:87]
	v_mfma_f32_16x16x32_f16 v[88:91], v[22:25], v[56:59], v[88:91]
	s_waitcnt lgkmcnt(0)
	v_mfma_f32_16x16x32_f16 v[84:87], v[34:37], v[60:63], v[84:87]
	v_mfma_f32_16x16x32_f16 v[88:91], v[26:29], v[60:63], v[88:91]
	ds_read_b128 v[44:47], v75 offset:2048
	ds_read_b128 v[68:71], v75 offset:3072
	s_nop 5
	v_exp_f32_e32 v94, v86
	v_exp_f32_e32 v95, v90
	v_exp_f32_e32 v96, v84
	v_exp_f32_e32 v97, v88
	v_exp_f32_e32 v98, v85
	v_exp_f32_e32 v99, v89
	v_pk_add_f32 v[100:101], v[94:95], 1.0 op_sel_hi:[1,0]
	v_pk_fma_f32 v[102:103], v[94:95], s[8:9], v[92:93] op_sel_hi:[1,0,0]
	v_pk_fma_f32 v[100:101], v[96:97], v[100:101], v[100:101]
	v_pk_fma_f32 v[104:105], v[100:101], v[98:99], v[100:101]
	v_rcp_f32_e32 v104, v104
	v_rcp_f32_e32 v105, v105
	v_pk_fma_f32 v[102:103], v[102:103], v[98:99], v[102:103]
	v_pk_fma_f32 v[102:103], v[64:65], v[100:101], v[102:103]
	v_exp_f32_e32 v106, v87
	v_pk_mul_f32 v[64:65], v[102:103], v[104:105]
	v_exp_f32_e32 v108, v64
	v_exp_f32_e32 v109, v65
	v_exp_f32_e32 v107, v91
	v_pk_add_f32 v[110:111], v[108:109], 1.0 op_sel_hi:[1,0]
	v_pk_fma_f32 v[110:111], v[110:111], v[106:107], v[110:111]
	v_rcp_f32_e32 v110, v110
	v_rcp_f32_e32 v111, v111
	v_pk_add_f32 v[112:113], v[108:109], -1.0 op_sel_hi:[1,0]
	v_pk_mul_f32 v[112:113], v[112:113], v[110:111]
	v_cvt_pk_f16_f32 v114, v112, v113
	ds_write_b32 v81, v114 offset:4096
	s_waitcnt lgkmcnt(1)
	v_mfma_f32_16x16x32_f16 v[84:87], v[2:5], v[44:47], v[18:21]
	v_mfma_f32_16x16x32_f16 v[88:91], v[14:17], v[44:47], v[38:41]
	v_mfma_f32_16x16x32_f16 v[84:87], v[6:9], v[68:71], v[84:87]
	v_mfma_f32_16x16x32_f16 v[88:91], v[10:13], v[68:71], v[88:91]
	s_waitcnt lgkmcnt(0)
	s_barrier
	ds_read_b128 v[56:59], v75 offset:4096
	ds_read_b128 v[60:63], v75 offset:5120
	s_waitcnt lgkmcnt(1)
	v_mfma_f32_16x16x32_f16 v[84:87], v[30:33], v[56:59], v[84:87]
	v_mfma_f32_16x16x32_f16 v[88:91], v[22:25], v[56:59], v[88:91]
	s_waitcnt lgkmcnt(0)
	v_mfma_f32_16x16x32_f16 v[84:87], v[34:37], v[60:63], v[84:87]
	v_mfma_f32_16x16x32_f16 v[88:91], v[26:29], v[60:63], v[88:91]
	ds_read_b128 v[44:47], v75 offset:0
	ds_read_b128 v[68:71], v75 offset:1024
	v_mfma_f32_16x16x32_f16 v[50:53], v[120:123], v[60:63], 0
	s_nop 5
	v_exp_f32_e32 v94, v86
	v_exp_f32_e32 v95, v90
	v_exp_f32_e32 v96, v84
	v_exp_f32_e32 v97, v88
	v_exp_f32_e32 v98, v85
	v_exp_f32_e32 v99, v89
	v_add_f32_e32 v125, v50, v51
	s_mov_b64 s[16:17], exec
	s_mov_b64 exec, s[30:31]
	ds_write_b32 v74, v125 offset:192
	s_mov_b64 exec, s[16:17]
	v_pk_add_f32 v[100:101], v[94:95], 1.0 op_sel_hi:[1,0]
	v_pk_fma_f32 v[102:103], v[94:95], s[8:9], v[92:93] op_sel_hi:[1,0,0]
	v_pk_fma_f32 v[100:101], v[96:97], v[100:101], v[100:101]
	v_pk_fma_f32 v[104:105], v[100:101], v[98:99], v[100:101]
	v_rcp_f32_e32 v104, v104
	v_rcp_f32_e32 v105, v105
	v_pk_fma_f32 v[102:103], v[102:103], v[98:99], v[102:103]
	v_pk_fma_f32 v[102:103], v[64:65], v[100:101], v[102:103]
	v_exp_f32_e32 v106, v87
	v_pk_mul_f32 v[64:65], v[102:103], v[104:105]
	v_exp_f32_e32 v108, v64
	v_exp_f32_e32 v109, v65
	v_exp_f32_e32 v107, v91
	v_pk_add_f32 v[110:111], v[108:109], 1.0 op_sel_hi:[1,0]
	v_pk_fma_f32 v[110:111], v[110:111], v[106:107], v[110:111]
	v_rcp_f32_e32 v110, v110
	v_rcp_f32_e32 v111, v111
	v_pk_add_f32 v[112:113], v[108:109], -1.0 op_sel_hi:[1,0]
	v_pk_mul_f32 v[112:113], v[112:113], v[110:111]
	v_cvt_pk_f16_f32 v114, v112, v113
	ds_write_b32 v81, v114 offset:6144
	s_waitcnt lgkmcnt(1)
	v_mfma_f32_16x16x32_f16 v[84:87], v[2:5], v[44:47], v[18:21]
	v_mfma_f32_16x16x32_f16 v[88:91], v[14:17], v[44:47], v[38:41]
	v_mfma_f32_16x16x32_f16 v[84:87], v[6:9], v[68:71], v[84:87]
	v_mfma_f32_16x16x32_f16 v[88:91], v[10:13], v[68:71], v[88:91]
	s_waitcnt lgkmcnt(0)
	.p2align	6
.Lcb1_loop:
	s_barrier
	ds_read_b128 v[56:59], v75 offset:6144
	ds_read_b128 v[60:63], v75 offset:7168
	s_waitcnt lgkmcnt(1)
	v_mfma_f32_16x16x32_f16 v[84:87], v[30:33], v[56:59], v[84:87]
	v_mfma_f32_16x16x32_f16 v[88:91], v[22:25], v[56:59], v[88:91]
	s_waitcnt lgkmcnt(0)
	v_mfma_f32_16x16x32_f16 v[84:87], v[34:37], v[60:63], v[84:87]
	v_mfma_f32_16x16x32_f16 v[88:91], v[26:29], v[60:63], v[88:91]
	ds_read_b128 v[44:47], v75 offset:2048
	ds_read_b128 v[68:71], v75 offset:3072
	v_mfma_f32_16x16x32_f16 v[50:53], v[120:123], v[60:63], 0
	s_nop 5
	v_exp_f32_e32 v94, v86
	v_exp_f32_e32 v95, v90
	v_exp_f32_e32 v96, v84
	v_exp_f32_e32 v97, v88
	v_exp_f32_e32 v98, v85
	v_exp_f32_e32 v99, v89
	v_add_f32_e32 v125, v50, v51
	s_mov_b64 s[16:17], exec
	s_mov_b64 exec, s[30:31]
	ds_write_b32 v74, v125 offset:64
	s_mov_b64 exec, s[16:17]
	v_pk_add_f32 v[100:101], v[94:95], 1.0 op_sel_hi:[1,0]
	v_pk_fma_f32 v[102:103], v[94:95], s[8:9], v[92:93] op_sel_hi:[1,0,0]
	v_pk_fma_f32 v[100:101], v[96:97], v[100:101], v[100:101]
	v_pk_fma_f32 v[104:105], v[100:101], v[98:99], v[100:101]
	v_rcp_f32_e32 v104, v104
	v_rcp_f32_e32 v105, v105
	v_pk_fma_f32 v[102:103], v[102:103], v[98:99], v[102:103]
	v_pk_fma_f32 v[102:103], v[64:65], v[100:101], v[102:103]
	v_exp_f32_e32 v106, v87
	v_pk_mul_f32 v[64:65], v[102:103], v[104:105]
	v_exp_f32_e32 v108, v64
	v_exp_f32_e32 v109, v65
	v_exp_f32_e32 v107, v91
	v_pk_add_f32 v[110:111], v[108:109], 1.0 op_sel_hi:[1,0]
	v_pk_fma_f32 v[110:111], v[110:111], v[106:107], v[110:111]
	v_rcp_f32_e32 v110, v110
	v_rcp_f32_e32 v111, v111
	v_pk_add_f32 v[112:113], v[108:109], -1.0 op_sel_hi:[1,0]
	v_pk_mul_f32 v[112:113], v[112:113], v[110:111]
	v_cvt_pk_f16_f32 v114, v112, v113
	ds_write_b32 v81, v114 offset:4096
	s_waitcnt lgkmcnt(1)
	v_mfma_f32_16x16x32_f16 v[84:87], v[2:5], v[44:47], v[18:21]
	v_mfma_f32_16x16x32_f16 v[88:91], v[14:17], v[44:47], v[38:41]
	v_mfma_f32_16x16x32_f16 v[84:87], v[6:9], v[68:71], v[84:87]
	v_mfma_f32_16x16x32_f16 v[88:91], v[10:13], v[68:71], v[88:91]
	s_waitcnt lgkmcnt(0)
	s_barrier
	ds_read_b128 v[56:59], v75 offset:4096
	ds_read_b128 v[60:63], v75 offset:5120
	s_waitcnt lgkmcnt(1)
	v_mfma_f32_16x16x32_f16 v[84:87], v[30:33], v[56:59], v[84:87]
	v_mfma_f32_16x16x32_f16 v[88:91], v[22:25], v[56:59], v[88:91]
	s_waitcnt lgkmcnt(0)
	v_mfma_f32_16x16x32_f16 v[84:87], v[34:37], v[60:63], v[84:87]
	v_mfma_f32_16x16x32_f16 v[88:91], v[26:29], v[60:63], v[88:91]
	ds_read_b128 v[44:47], v75 offset:0
	ds_read_b128 v[68:71], v75 offset:1024
	v_mfma_f32_16x16x32_f16 v[50:53], v[120:123], v[60:63], 0
	s_nop 5
	v_exp_f32_e32 v94, v86
	v_exp_f32_e32 v95, v90
	v_exp_f32_e32 v96, v84
	v_exp_f32_e32 v97, v88
	v_exp_f32_e32 v98, v85
	v_exp_f32_e32 v99, v89
	v_add_f32_e32 v125, v50, v51
	s_mov_b64 s[16:17], exec
	s_mov_b64 exec, s[30:31]
	ds_write_b32 v74, v125 offset:192
	s_mov_b64 exec, s[16:17]
	v_pk_add_f32 v[100:101], v[94:95], 1.0 op_sel_hi:[1,0]
	v_pk_fma_f32 v[102:103], v[94:95], s[8:9], v[92:93] op_sel_hi:[1,0,0]
	v_pk_fma_f32 v[100:101], v[96:97], v[100:101], v[100:101]
	v_pk_fma_f32 v[104:105], v[100:101], v[98:99], v[100:101]
	v_rcp_f32_e32 v104, v104
	v_rcp_f32_e32 v105, v105
	v_pk_fma_f32 v[102:103], v[102:103], v[98:99], v[102:103]
	v_pk_fma_f32 v[102:103], v[64:65], v[100:101], v[102:103]
	v_exp_f32_e32 v106, v87
	v_pk_mul_f32 v[64:65], v[102:103], v[104:105]
	v_exp_f32_e32 v108, v64
	v_exp_f32_e32 v109, v65
	v_exp_f32_e32 v107, v91
	v_pk_add_f32 v[110:111], v[108:109], 1.0 op_sel_hi:[1,0]
	v_pk_fma_f32 v[110:111], v[110:111], v[106:107], v[110:111]
	v_rcp_f32_e32 v110, v110
	v_rcp_f32_e32 v111, v111
	v_pk_add_f32 v[112:113], v[108:109], -1.0 op_sel_hi:[1,0]
	v_pk_mul_f32 v[112:113], v[112:113], v[110:111]
	v_cvt_pk_f16_f32 v114, v112, v113
	ds_write_b32 v81, v114 offset:6144
	s_waitcnt lgkmcnt(1)
	v_mfma_f32_16x16x32_f16 v[84:87], v[2:5], v[44:47], v[18:21]
	v_mfma_f32_16x16x32_f16 v[88:91], v[14:17], v[44:47], v[38:41]
	v_mfma_f32_16x16x32_f16 v[84:87], v[6:9], v[68:71], v[84:87]
	v_mfma_f32_16x16x32_f16 v[88:91], v[10:13], v[68:71], v[88:91]
	s_waitcnt lgkmcnt(0)
	s_barrier
	ds_read_b128 v[56:59], v75 offset:6144
	ds_read_b128 v[60:63], v75 offset:7168
	s_waitcnt lgkmcnt(1)
	v_mfma_f32_16x16x32_f16 v[84:87], v[30:33], v[56:59], v[84:87]
	v_mfma_f32_16x16x32_f16 v[88:91], v[22:25], v[56:59], v[88:91]
	s_waitcnt lgkmcnt(0)
	v_mfma_f32_16x16x32_f16 v[84:87], v[34:37], v[60:63], v[84:87]
	v_mfma_f32_16x16x32_f16 v[88:91], v[26:29], v[60:63], v[88:91]
	ds_read_b128 v[44:47], v75 offset:2048
	ds_read_b128 v[68:71], v75 offset:3072
	v_mfma_f32_16x16x32_f16 v[50:53], v[120:123], v[60:63], 0
	s_nop 5
	v_exp_f32_e32 v94, v86
	v_exp_f32_e32 v95, v90
	v_exp_f32_e32 v96, v84
	v_exp_f32_e32 v97, v88
	v_exp_f32_e32 v98, v85
	v_exp_f32_e32 v99, v89
	v_add_f32_e32 v125, v50, v51
	s_mov_b64 s[16:17], exec
	s_mov_b64 exec, s[30:31]
	ds_write_b32 v74, v125 offset:64
	s_mov_b64 exec, s[16:17]
	v_pk_add_f32 v[100:101], v[94:95], 1.0 op_sel_hi:[1,0]
	v_pk_fma_f32 v[102:103], v[94:95], s[8:9], v[92:93] op_sel_hi:[1,0,0]
	v_pk_fma_f32 v[100:101], v[96:97], v[100:101], v[100:101]
	v_pk_fma_f32 v[104:105], v[100:101], v[98:99], v[100:101]
	v_rcp_f32_e32 v104, v104
	v_rcp_f32_e32 v105, v105
	v_pk_fma_f32 v[102:103], v[102:103], v[98:99], v[102:103]
	v_pk_fma_f32 v[102:103], v[64:65], v[100:101], v[102:103]
	v_exp_f32_e32 v106, v87
	v_pk_mul_f32 v[64:65], v[102:103], v[104:105]
	v_exp_f32_e32 v108, v64
	v_exp_f32_e32 v109, v65
	v_exp_f32_e32 v107, v91
	v_pk_add_f32 v[110:111], v[108:109], 1.0 op_sel_hi:[1,0]
	v_pk_fma_f32 v[110:111], v[110:111], v[106:107], v[110:111]
	v_rcp_f32_e32 v110, v110
	v_rcp_f32_e32 v111, v111
	v_pk_add_f32 v[112:113], v[108:109], -1.0 op_sel_hi:[1,0]
	v_pk_mul_f32 v[112:113], v[112:113], v[110:111]
	v_cvt_pk_f16_f32 v114, v112, v113
	ds_write_b32 v81, v114 offset:4096
	s_waitcnt lgkmcnt(1)
	v_mfma_f32_16x16x32_f16 v[84:87], v[2:5], v[44:47], v[18:21]
	v_mfma_f32_16x16x32_f16 v[88:91], v[14:17], v[44:47], v[38:41]
	v_mfma_f32_16x16x32_f16 v[84:87], v[6:9], v[68:71], v[84:87]
	v_mfma_f32_16x16x32_f16 v[88:91], v[10:13], v[68:71], v[88:91]
	s_waitcnt lgkmcnt(0)
	s_barrier
	ds_read_b128 v[56:59], v75 offset:4096
	ds_read_b128 v[60:63], v75 offset:5120
	s_waitcnt lgkmcnt(1)
	v_mfma_f32_16x16x32_f16 v[84:87], v[30:33], v[56:59], v[84:87]
	v_mfma_f32_16x16x32_f16 v[88:91], v[22:25], v[56:59], v[88:91]
	s_waitcnt lgkmcnt(0)
	v_mfma_f32_16x16x32_f16 v[84:87], v[34:37], v[60:63], v[84:87]
	v_mfma_f32_16x16x32_f16 v[88:91], v[26:29], v[60:63], v[88:91]
	ds_read_b128 v[44:47], v75 offset:0
	ds_read_b128 v[68:71], v75 offset:1024
	v_mfma_f32_16x16x32_f16 v[50:53], v[120:123], v[60:63], 0
	s_nop 5
	v_exp_f32_e32 v94, v86
	v_exp_f32_e32 v95, v90
	v_exp_f32_e32 v96, v84
	v_exp_f32_e32 v97, v88
	v_exp_f32_e32 v98, v85
	v_exp_f32_e32 v99, v89
	v_add_f32_e32 v125, v50, v51
	s_mov_b64 s[16:17], exec
	s_mov_b64 exec, s[30:31]
	ds_write_b32 v74, v125 offset:192
	s_mov_b64 exec, s[16:17]
	v_pk_add_f32 v[100:101], v[94:95], 1.0 op_sel_hi:[1,0]
	v_pk_fma_f32 v[102:103], v[94:95], s[8:9], v[92:93] op_sel_hi:[1,0,0]
	v_pk_fma_f32 v[100:101], v[96:97], v[100:101], v[100:101]
	v_pk_fma_f32 v[104:105], v[100:101], v[98:99], v[100:101]
	v_rcp_f32_e32 v104, v104
	v_rcp_f32_e32 v105, v105
	v_pk_fma_f32 v[102:103], v[102:103], v[98:99], v[102:103]
	v_pk_fma_f32 v[102:103], v[64:65], v[100:101], v[102:103]
	v_exp_f32_e32 v106, v87
	v_pk_mul_f32 v[64:65], v[102:103], v[104:105]
	v_exp_f32_e32 v108, v64
	v_exp_f32_e32 v109, v65
	v_exp_f32_e32 v107, v91
	v_pk_add_f32 v[110:111], v[108:109], 1.0 op_sel_hi:[1,0]
	v_pk_fma_f32 v[110:111], v[110:111], v[106:107], v[110:111]
	v_rcp_f32_e32 v110, v110
	v_rcp_f32_e32 v111, v111
	v_pk_add_f32 v[112:113], v[108:109], -1.0 op_sel_hi:[1,0]
	v_pk_mul_f32 v[112:113], v[112:113], v[110:111]
	v_cvt_pk_f16_f32 v114, v112, v113
	ds_write_b32 v81, v114 offset:6144
	s_waitcnt lgkmcnt(1)
	v_mfma_f32_16x16x32_f16 v[84:87], v[2:5], v[44:47], v[18:21]
	v_mfma_f32_16x16x32_f16 v[88:91], v[14:17], v[44:47], v[38:41]
	v_mfma_f32_16x16x32_f16 v[84:87], v[6:9], v[68:71], v[84:87]
	v_mfma_f32_16x16x32_f16 v[88:91], v[10:13], v[68:71], v[88:91]
	s_waitcnt lgkmcnt(0)
	v_min_f32_e32 v64, 0x42700000, v64
	v_min_f32_e32 v65, 0x42700000, v65
	s_add_u32 s12, s12, 4
	v_add_u32_e32 v124, 16, v124
	s_cmp_lt_u32 s12, 452
	s_cbranch_scc1 .Lcb1_loop
	s_barrier
	ds_read_b128 v[56:59], v75 offset:6144
	ds_read_b128 v[60:63], v75 offset:7168
	s_waitcnt lgkmcnt(0)
	v_mfma_f32_16x16x32_f16 v[50:53], v[120:123], v[60:63], 0
	s_nop 7
	v_add_f32_e32 v125, v50, v51
	s_mov_b64 s[16:17], exec
	s_mov_b64 exec, s[30:31]
	ds_write_b32 v74, v125 offset:64
	s_mov_b64 exec, s[16:17]
	s_waitcnt lgkmcnt(0)
	s_barrier
	s_waitcnt lgkmcnt(0)
	s_endpgm
.Lcb_r2:
	s_barrier
	ds_read_b128 v[44:47], v75 offset:0
	ds_read_b128 v[68:71], v75 offset:1024
	s_waitcnt lgkmcnt(0)
	v_mfma_f32_16x16x32_f16 v[84:87], v[2:5], v[44:47], v[18:21]
	v_mfma_f32_16x16x32_f16 v[88:91], v[14:17], v[44:47], v[38:41]
	v_mfma_f32_16x16x32_f16 v[84:87], v[6:9], v[68:71], v[84:87]
	v_mfma_f32_16x16x32_f16 v[88:91], v[10:13], v[68:71], v[88:91]
	s_barrier
	ds_read_b128 v[56:59], v75 offset:6144
	ds_read_b128 v[60:63], v75 offset:7168
	s_waitcnt lgkmcnt(1)
	v_mfma_f32_16x16x32_f16 v[84:87], v[30:33], v[56:59], v[84:87]
	v_mfma_f32_16x16x32_f16 v[88:91], v[22:25], v[56:59], v[88:91]
	s_waitcnt lgkmcnt(0)
	v_mfma_f32_16x16x32_f16 v[84:87], v[34:37], v[60:63], v[84:87]
	v_mfma_f32_16x16x32_f16 v[88:91], v[26:29], v[60:63], v[88:91]
	ds_read_b128 v[44:47], v75 offset:2048
	ds_read_b128 v[68:71], v75 offset:3072
	s_nop 5
	v_exp_f32_e32 v94, v86
	v_exp_f32_e32 v95, v90
	v_exp_f32_e32 v96, v84
	v_exp_f32_e32 v97, v88
	v_exp_f32_e32 v98, v85
	v_exp_f32_e32 v99, v89
	v_pk_add_f32 v[100:101], v[94:95], 1.0 op_sel_hi:[1,0]
	v_pk_fma_f32 v[102:103], v[94:95], s[8:9], v[92:93] op_sel_hi:[1,0,0]
	v_pk_fma_f32 v[100:101], v[96:97], v[100:101], v[100:101]
	v_pk_fma_f32 v[104:105], v[100:101], v[98:99], v[100:101]
	v_rcp_f32_e32 v104, v104
	v_rcp_f32_e32 v105, v105
	v_pk_fma_f32 v[102:103], v[102:103], v[98:99], v[102:103]
	v_pk_fma_f32 v[102:103], v[64:65], v[100:101], v[102:103]
	v_exp_f32_e32 v106, v87
	v_pk_mul_f32 v[64:65], v[102:103], v[104:105]
	v_exp_f32_e32 v108, v64
	v_exp_f32_e32 v109, v65
	v_exp_f32_e32 v107, v91
	v_pk_add_f32 v[110:111], v[108:109], 1.0 op_sel_hi:[1,0]
	v_pk_fma_f32 v[110:111], v[110:111], v[106:107], v[110:111]
	v_rcp_f32_e32 v110, v110
	v_rcp_f32_e32 v111, v111
	v_pk_add_f32 v[112:113], v[108:109], -1.0 op_sel_hi:[1,0]
	v_pk_mul_f32 v[112:113], v[112:113], v[110:111]
	v_cvt_pk_f16_f32 v114, v112, v113
	ds_write_b32 v81, v114 offset:4096
	s_waitcnt lgkmcnt(1)
	v_mfma_f32_16x16x32_f16 v[84:87], v[2:5], v[44:47], v[18:21]
	v_mfma_f32_16x16x32_f16 v[88:91], v[14:17], v[44:47], v[38:41]
	v_mfma_f32_16x16x32_f16 v[84:87], v[6:9], v[68:71], v[84:87]
	v_mfma_f32_16x16x32_f16 v[88:91], v[10:13], v[68:71], v[88:91]
	s_waitcnt lgkmcnt(0)
	s_barrier
	ds_read_b128 v[56:59], v75 offset:4096
	ds_read_b128 v[60:63], v75 offset:5120
	s_waitcnt lgkmcnt(1)
	v_mfma_f32_16x16x32_f16 v[84:87], v[30:33], v[56:59], v[84:87]
	v_mfma_f32_16x16x32_f16 v[88:91], v[22:25], v[56:59], v[88:91]
	s_waitcnt lgkmcnt(0)
	v_mfma_f32_16x16x32_f16 v[84:87], v[34:37], v[60:63], v[84:87]
	v_mfma_f32_16x16x32_f16 v[88:91], v[26:29], v[60:63], v[88:91]
	ds_read_b128 v[44:47], v75 offset:0
	ds_read_b128 v[68:71], v75 offset:1024
	s_nop 5
	v_exp_f32_e32 v94, v86
	v_exp_f32_e32 v95, v90
	v_exp_f32_e32 v96, v84
	v_exp_f32_e32 v97, v88
	v_exp_f32_e32 v98, v85
	v_exp_f32_e32 v99, v89
	v_pk_add_f32 v[100:101], v[94:95], 1.0 op_sel_hi:[1,0]
	v_pk_fma_f32 v[102:103], v[94:95], s[8:9], v[92:93] op_sel_hi:[1,0,0]
	v_pk_fma_f32 v[100:101], v[96:97], v[100:101], v[100:101]
	v_pk_fma_f32 v[104:105], v[100:101], v[98:99], v[100:101]
	v_rcp_f32_e32 v104, v104
	v_rcp_f32_e32 v105, v105
	v_pk_fma_f32 v[102:103], v[102:103], v[98:99], v[102:103]
	v_pk_fma_f32 v[102:103], v[64:65], v[100:101], v[102:103]
	v_exp_f32_e32 v106, v87
	v_pk_mul_f32 v[64:65], v[102:103], v[104:105]
	v_exp_f32_e32 v108, v64
	v_exp_f32_e32 v109, v65
	v_exp_f32_e32 v107, v91
	v_pk_add_f32 v[110:111], v[108:109], 1.0 op_sel_hi:[1,0]
	v_pk_fma_f32 v[110:111], v[110:111], v[106:107], v[110:111]
	v_rcp_f32_e32 v110, v110
	v_rcp_f32_e32 v111, v111
	v_pk_add_f32 v[112:113], v[108:109], -1.0 op_sel_hi:[1,0]
	v_pk_mul_f32 v[112:113], v[112:113], v[110:111]
	v_cvt_pk_f16_f32 v114, v112, v113
	ds_write_b32 v81, v114 offset:6144
	s_waitcnt lgkmcnt(1)
	v_mfma_f32_16x16x32_f16 v[84:87], v[2:5], v[44:47], v[18:21]
	v_mfma_f32_16x16x32_f16 v[88:91], v[14:17], v[44:47], v[38:41]
	v_mfma_f32_16x16x32_f16 v[84:87], v[6:9], v[68:71], v[84:87]
	v_mfma_f32_16x16x32_f16 v[88:91], v[10:13], v[68:71], v[88:91]
	s_waitcnt lgkmcnt(0)
	.p2align	6
.Lcb2_loop:
	s_barrier
	ds_read_b32 v125, v74 offset:128
	ds_read_b32 v126, v74 offset:192
	ds_read_b128 v[56:59], v75 offset:6144
	ds_read_b128 v[60:63], v75 offset:7168
	s_waitcnt lgkmcnt(2)
	v_add_f32_e32 v125, v125, v126
	v_mul_f32_e32 v126, 0x3fb8aa3b, v125
	v_exp_f32_e32 v126, v126
	v_cmp_lt_f32_e32 vcc, 0, v125
	v_mul_f32_e32 v125, 0x3f867d5f, v125
	v_fma_f32 v126, v126, v72, v73
	s_nop 0
	v_cndmask_b32_e32 v125, v126, v125, vcc
	s_mov_b64 s[16:17], exec
	s_mov_b64 exec, s[30:31]
	global_store_dword v124, v125, s[26:27] offset:0
	s_mov_b64 exec, s[16:17]
	s_waitcnt lgkmcnt(1)
	v_mfma_f32_16x16x32_f16 v[84:87], v[30:33], v[56:59], v[84:87]
	v_mfma_f32_16x16x32_f16 v[88:91], v[22:25], v[56:59], v[88:91]
	s_waitcnt lgkmcnt(0)
	v_mfma_f32_16x16x32_f16 v[84:87], v[34:37], v[60:63], v[84:87]
	v_mfma_f32_16x16x32_f16 v[88:91], v[26:29], v[60:63], v[88:91]
	ds_read_b128 v[44:47], v75 offset:2048
	ds_read_b128 v[68:71], v75 offset:3072
	s_nop 5
	v_exp_f32_e32 v94, v86
	v_exp_f32_e32 v95, v90
	v_exp_f32_e32 v96, v84
	v_exp_f32_e32 v97, v88
	v_exp_f32_e32 v98, v85
	v_exp_f32_e32 v99, v89
	v_pk_add_f32 v[100:101], v[94:95], 1.0 op_sel_hi:[1,0]
	v_pk_fma_f32 v[102:103], v[94:95], s[8:9], v[92:93] op_sel_hi:[1,0,0]
	v_pk_fma_f32 v[100:101], v[96:97], v[100:101], v[100:101]
	v_pk_fma_f32 v[104:105], v[100:101], v[98:99], v[100:101]
	v_rcp_f32_e32 v104, v104
	v_rcp_f32_e32 v105, v105
	v_pk_fma_f32 v[102:103], v[102:103], v[98:99], v[102:103]
	v_pk_fma_f32 v[102:103], v[64:65], v[100:101], v[102:103]
	v_exp_f32_e32 v106, v87
	v_pk_mul_f32 v[64:65], v[102:103], v[104:105]
	v_exp_f32_e32 v108, v64
	v_exp_f32_e32 v109, v65
	v_exp_f32_e32 v107, v91
	v_pk_add_f32 v[110:111], v[108:109], 1.0 op_sel_hi:[1,0]
	v_pk_fma_f32 v[110:111], v[110:111], v[106:107], v[110:111]
	v_rcp_f32_e32 v110, v110
	v_rcp_f32_e32 v111, v111
	v_pk_add_f32 v[112:113], v[108:109], -1.0 op_sel_hi:[1,0]
	v_pk_mul_f32 v[112:113], v[112:113], v[110:111]
	v_cvt_pk_f16_f32 v114, v112, v113
	ds_write_b32 v81, v114 offset:4096
	s_waitcnt lgkmcnt(1)
	v_mfma_f32_16x16x32_f16 v[84:87], v[2:5], v[44:47], v[18:21]
	v_mfma_f32_16x16x32_f16 v[88:91], v[14:17], v[44:47], v[38:41]
	v_mfma_f32_16x16x32_f16 v[84:87], v[6:9], v[68:71], v[84:87]
	v_mfma_f32_16x16x32_f16 v[88:91], v[10:13], v[68:71], v[88:91]
	s_waitcnt lgkmcnt(0)
	s_barrier
	ds_read_b32 v125, v74 offset:0
	ds_read_b32 v126, v74 offset:64
	ds_read_b128 v[56:59], v75 offset:4096
	ds_read_b128 v[60:63], v75 offset:5120
	s_waitcnt lgkmcnt(2)
	v_add_f32_e32 v125, v125, v126
	v_mul_f32_e32 v126, 0x3fb8aa3b, v125
	v_exp_f32_e32 v126, v126
	v_cmp_lt_f32_e32 vcc, 0, v125
	v_mul_f32_e32 v125, 0x3f867d5f, v125
	v_fma_f32 v126, v126, v72, v73
	s_nop 0
	v_cndmask_b32_e32 v125, v126, v125, vcc
	s_mov_b64 s[16:17], exec
	s_mov_b64 exec, s[30:31]
	global_store_dword v124, v125, s[26:27] offset:4
	s_mov_b64 exec, s[16:17]
	s_waitcnt lgkmcnt(1)
	v_mfma_f32_16x16x32_f16 v[84:87], v[30:33], v[56:59], v[84:87]
	v_mfma_f32_16x16x32_f16 v[88:91], v[22:25], v[56:59], v[88:91]
	s_waitcnt lgkmcnt(0)
	v_mfma_f32_16x16x32_f16 v[84:87], v[34:37], v[60:63], v[84:87]
	v_mfma_f32_16x16x32_f16 v[88:91], v[26:29], v[60:63], v[88:91]
	ds_read_b128 v[44:47], v75 offset:0
	ds_read_b128 v[68:71], v75 offset:1024
	s_nop 5
	v_exp_f32_e32 v94, v86
	v_exp_f32_e32 v95, v90
	v_exp_f32_e32 v96, v84
	v_exp_f32_e32 v97, v88
	v_exp_f32_e32 v98, v85
	v_exp_f32_e32 v99, v89
	v_pk_add_f32 v[100:101], v[94:95], 1.0 op_sel_hi:[1,0]
	v_pk_fma_f32 v[102:103], v[94:95], s[8:9], v[92:93] op_sel_hi:[1,0,0]
	v_pk_fma_f32 v[100:101], v[96:97], v[100:101], v[100:101]
	v_pk_fma_f32 v[104:105], v[100:101], v[98:99], v[100:101]
	v_rcp_f32_e32 v104, v104
	v_rcp_f32_e32 v105, v105
	v_pk_fma_f32 v[102:103], v[102:103], v[98:99], v[102:103]
	v_pk_fma_f32 v[102:103], v[64:65], v[100:101], v[102:103]
	v_exp_f32_e32 v106, v87
	v_pk_mul_f32 v[64:65], v[102:103], v[104:105]
	v_exp_f32_e32 v108, v64
	v_exp_f32_e32 v109, v65
	v_exp_f32_e32 v107, v91
	v_pk_add_f32 v[110:111], v[108:109], 1.0 op_sel_hi:[1,0]
	v_pk_fma_f32 v[110:111], v[110:111], v[106:107], v[110:111]
	v_rcp_f32_e32 v110, v110
	v_rcp_f32_e32 v111, v111
	v_pk_add_f32 v[112:113], v[108:109], -1.0 op_sel_hi:[1,0]
	v_pk_mul_f32 v[112:113], v[112:113], v[110:111]
	v_cvt_pk_f16_f32 v114, v112, v113
	ds_write_b32 v81, v114 offset:6144
	s_waitcnt lgkmcnt(1)
	v_mfma_f32_16x16x32_f16 v[84:87], v[2:5], v[44:47], v[18:21]
	v_mfma_f32_16x16x32_f16 v[88:91], v[14:17], v[44:47], v[38:41]
	v_mfma_f32_16x16x32_f16 v[84:87], v[6:9], v[68:71], v[84:87]
	v_mfma_f32_16x16x32_f16 v[88:91], v[10:13], v[68:71], v[88:91]
	s_waitcnt lgkmcnt(0)
	s_barrier
	ds_read_b32 v125, v74 offset:128
	ds_read_b32 v126, v74 offset:192
	ds_read_b128 v[56:59], v75 offset:6144
	ds_read_b128 v[60:63], v75 offset:7168
	s_waitcnt lgkmcnt(2)
	v_add_f32_e32 v125, v125, v126
	v_mul_f32_e32 v126, 0x3fb8aa3b, v125
	v_exp_f32_e32 v126, v126
	v_cmp_lt_f32_e32 vcc, 0, v125
	v_mul_f32_e32 v125, 0x3f867d5f, v125
	v_fma_f32 v126, v126, v72, v73
	s_nop 0
	v_cndmask_b32_e32 v125, v126, v125, vcc
	s_mov_b64 s[16:17], exec
	s_mov_b64 exec, s[30:31]
	global_store_dword v124, v125, s[26:27] offset:8
	s_mov_b64 exec, s[16:17]
	s_waitcnt lgkmcnt(1)
	v_mfma_f32_16x16x32_f16 v[84:87], v[30:33], v[56:59], v[84:87]
	v_mfma_f32_16x16x32_f16 v[88:91], v[22:25], v[56:59], v[88:91]
	s_waitcnt lgkmcnt(0)
	v_mfma_f32_16x16x32_f16 v[84:87], v[34:37], v[60:63], v[84:87]
	v_mfma_f32_16x16x32_f16 v[88:91], v[26:29], v[60:63], v[88:91]
	ds_read_b128 v[44:47], v75 offset:2048
	ds_read_b128 v[68:71], v75 offset:3072
	s_nop 5
	v_exp_f32_e32 v94, v86
	v_exp_f32_e32 v95, v90
	v_exp_f32_e32 v96, v84
	v_exp_f32_e32 v97, v88
	v_exp_f32_e32 v98, v85
	v_exp_f32_e32 v99, v89
	v_pk_add_f32 v[100:101], v[94:95], 1.0 op_sel_hi:[1,0]
	v_pk_fma_f32 v[102:103], v[94:95], s[8:9], v[92:93] op_sel_hi:[1,0,0]
	v_pk_fma_f32 v[100:101], v[96:97], v[100:101], v[100:101]
	v_pk_fma_f32 v[104:105], v[100:101], v[98:99], v[100:101]
	v_rcp_f32_e32 v104, v104
	v_rcp_f32_e32 v105, v105
	v_pk_fma_f32 v[102:103], v[102:103], v[98:99], v[102:103]
	v_pk_fma_f32 v[102:103], v[64:65], v[100:101], v[102:103]
	v_exp_f32_e32 v106, v87
	v_pk_mul_f32 v[64:65], v[102:103], v[104:105]
	v_exp_f32_e32 v108, v64
	v_exp_f32_e32 v109, v65
	v_exp_f32_e32 v107, v91
	v_pk_add_f32 v[110:111], v[108:109], 1.0 op_sel_hi:[1,0]
	v_pk_fma_f32 v[110:111], v[110:111], v[106:107], v[110:111]
	v_rcp_f32_e32 v110, v110
	v_rcp_f32_e32 v111, v111
	v_pk_add_f32 v[112:113], v[108:109], -1.0 op_sel_hi:[1,0]
	v_pk_mul_f32 v[112:113], v[112:113], v[110:111]
	v_cvt_pk_f16_f32 v114, v112, v113
	ds_write_b32 v81, v114 offset:4096
	s_waitcnt lgkmcnt(1)
	v_mfma_f32_16x16x32_f16 v[84:87], v[2:5], v[44:47], v[18:21]
	v_mfma_f32_16x16x32_f16 v[88:91], v[14:17], v[44:47], v[38:41]
	v_mfma_f32_16x16x32_f16 v[84:87], v[6:9], v[68:71], v[84:87]
	v_mfma_f32_16x16x32_f16 v[88:91], v[10:13], v[68:71], v[88:91]
	s_waitcnt lgkmcnt(0)
	s_barrier
	ds_read_b32 v125, v74 offset:0
	ds_read_b32 v126, v74 offset:64
	ds_read_b128 v[56:59], v75 offset:4096
	ds_read_b128 v[60:63], v75 offset:5120
	s_waitcnt lgkmcnt(2)
	v_add_f32_e32 v125, v125, v126
	v_mul_f32_e32 v126, 0x3fb8aa3b, v125
	v_exp_f32_e32 v126, v126
	v_cmp_lt_f32_e32 vcc, 0, v125
	v_mul_f32_e32 v125, 0x3f867d5f, v125
	v_fma_f32 v126, v126, v72, v73
	s_nop 0
	v_cndmask_b32_e32 v125, v126, v125, vcc
	s_mov_b64 s[16:17], exec
	s_mov_b64 exec, s[30:31]
	global_store_dword v124, v125, s[26:27] offset:12
	s_mov_b64 exec, s[16:17]
	s_waitcnt lgkmcnt(1)
	v_mfma_f32_16x16x32_f16 v[84:87], v[30:33], v[56:59], v[84:87]
	v_mfma_f32_16x16x32_f16 v[88:91], v[22:25], v[56:59], v[88:91]
	s_waitcnt lgkmcnt(0)
	v_mfma_f32_16x16x32_f16 v[84:87], v[34:37], v[60:63], v[84:87]
	v_mfma_f32_16x16x32_f16 v[88:91], v[26:29], v[60:63], v[88:91]
	ds_read_b128 v[44:47], v75 offset:0
	ds_read_b128 v[68:71], v75 offset:1024
	s_nop 5
	v_exp_f32_e32 v94, v86
	v_exp_f32_e32 v95, v90
	v_exp_f32_e32 v96, v84
	v_exp_f32_e32 v97, v88
	v_exp_f32_e32 v98, v85
	v_exp_f32_e32 v99, v89
	v_pk_add_f32 v[100:101], v[94:95], 1.0 op_sel_hi:[1,0]
	v_pk_fma_f32 v[102:103], v[94:95], s[8:9], v[92:93] op_sel_hi:[1,0,0]
	v_pk_fma_f32 v[100:101], v[96:97], v[100:101], v[100:101]
	v_pk_fma_f32 v[104:105], v[100:101], v[98:99], v[100:101]
	v_rcp_f32_e32 v104, v104
	v_rcp_f32_e32 v105, v105
	v_pk_fma_f32 v[102:103], v[102:103], v[98:99], v[102:103]
	v_pk_fma_f32 v[102:103], v[64:65], v[100:101], v[102:103]
	v_exp_f32_e32 v106, v87
	v_pk_mul_f32 v[64:65], v[102:103], v[104:105]
	v_exp_f32_e32 v108, v64
	v_exp_f32_e32 v109, v65
	v_exp_f32_e32 v107, v91
	v_pk_add_f32 v[110:111], v[108:109], 1.0 op_sel_hi:[1,0]
	v_pk_fma_f32 v[110:111], v[110:111], v[106:107], v[110:111]
	v_rcp_f32_e32 v110, v110
	v_rcp_f32_e32 v111, v111
	v_pk_add_f32 v[112:113], v[108:109], -1.0 op_sel_hi:[1,0]
	v_pk_mul_f32 v[112:113], v[112:113], v[110:111]
	v_cvt_pk_f16_f32 v114, v112, v113
	ds_write_b32 v81, v114 offset:6144
	s_waitcnt lgkmcnt(1)
	v_mfma_f32_16x16x32_f16 v[84:87], v[2:5], v[44:47], v[18:21]
	v_mfma_f32_16x16x32_f16 v[88:91], v[14:17], v[44:47], v[38:41]
	v_mfma_f32_16x16x32_f16 v[84:87], v[6:9], v[68:71], v[84:87]
	v_mfma_f32_16x16x32_f16 v[88:91], v[10:13], v[68:71], v[88:91]
	s_waitcnt lgkmcnt(0)
	v_min_f32_e32 v64, 0x42700000, v64
	v_min_f32_e32 v65, 0x42700000, v65
	s_add_u32 s12, s12, 4
	v_add_u32_e32 v124, 16, v124
	s_cmp_lt_u32 s12, 452
	s_cbranch_scc1 .Lcb2_loop
	s_barrier
	ds_read_b32 v125, v74 offset:128
	ds_read_b32 v126, v74 offset:192
	ds_read_b128 v[56:59], v75 offset:6144
	ds_read_b128 v[60:63], v75 offset:7168
	s_waitcnt lgkmcnt(2)
	v_add_f32_e32 v125, v125, v126
	v_mul_f32_e32 v126, 0x3fb8aa3b, v125
	v_exp_f32_e32 v126, v126
	v_cmp_lt_f32_e32 vcc, 0, v125
	v_mul_f32_e32 v125, 0x3f867d5f, v125
	v_fma_f32 v126, v126, v72, v73
	s_nop 0
	v_cndmask_b32_e32 v125, v126, v125, vcc
	s_mov_b64 s[16:17], exec
	s_mov_b64 exec, s[30:31]
	global_store_dword v124, v125, s[26:27] offset:0
	s_mov_b64 exec, s[16:17]
	s_waitcnt lgkmcnt(0)
	s_waitcnt lgkmcnt(0)
	s_barrier
	ds_read_b32 v125, v74 offset:0
	ds_read_b32 v126, v74 offset:64
	s_waitcnt lgkmcnt(0)
	v_add_f32_e32 v125, v125, v126
	v_mul_f32_e32 v126, 0x3fb8aa3b, v125
	v_exp_f32_e32 v126, v126
	v_cmp_lt_f32_e32 vcc, 0, v125
	v_mul_f32_e32 v125, 0x3f867d5f, v125
	v_fma_f32 v126, v126, v72, v73
	s_nop 0
	v_cndmask_b32_e32 v125, v126, v125, vcc
	s_mov_b64 s[16:17], exec
	s_mov_b64 exec, s[30:31]
	global_store_dword v124, v125, s[26:27] offset:4
	s_mov_b64 exec, s[16:17]
	s_waitcnt lgkmcnt(0)
	s_endpgm

.Lk_144:
	v_or_b32_e32 v46, 0x400, v54
	buffer_load_dwordx4 v[46:49], v46, s[4:7], 0 offen sc1
	ds_read_b128 v[50:53], v1
	v_mov_b32_e32 v66, 0
	v_add_u32_e32 v63, 0x800, v54
	s_mov_b32 s9, 0
	v_mov_b32_e32 v67, 0
	v_mov_b32_e32 v68, 0
	v_mov_b32_e32 v62, 0xc038aa3b
	s_mov_b32 s8, 0x4038aa3b
	v_mov_b32_e32 v65, 0
	v_mov_b32_e32 v64, v66
	s_setprio 2
	v_mov_b32_e32 v92, 0xc038aa3b
	v_mov_b32_e32 v93, 0xc038aa3b
	s_mov_b32 s8, 0x4038aa3b
	s_mov_b32 s9, 0
	v_mov_b32_e32 v64, 0
	v_mov_b32_e32 v65, 0
	v_mov_b32_e32 v66, 0
	v_mov_b32_e32 v67, 0
	v_mov_b32_e32 v68, 0
	v_mov_b32_e32 v116, v1
	v_mov_b32_e32 v117, v63
	s_mov_b32 s12, 0
	s_waitcnt lgkmcnt(0)
	s_setprio 2
	v_mfma_f32_16x16x32_f16 v[84:87], v[6:9], v[50:53], v[18:21]
	v_mfma_f32_16x16x32_f16 v[88:91], v[10:13], v[50:53], v[38:41]
	ds_read_b128 v[56:59], v75 offset:2048
	ds_read_b128 v[60:63], v75 offset:3072
	s_waitcnt vmcnt(1)
	v_mfma_f32_16x16x32_f16 v[84:87], v[2:5], v[42:45], v[84:87]
	v_mfma_f32_16x16x32_f16 v[88:91], v[14:17], v[42:45], v[88:91]
	s_waitcnt lgkmcnt(1)
	v_mfma_f32_16x16x32_f16 v[84:87], v[30:33], v[56:59], v[84:87]
	v_mfma_f32_16x16x32_f16 v[88:91], v[22:25], v[56:59], v[88:91]
	s_waitcnt lgkmcnt(0)
	v_mfma_f32_16x16x32_f16 v[84:87], v[34:37], v[60:63], v[84:87]
	v_mfma_f32_16x16x32_f16 v[88:91], v[26:29], v[60:63], v[88:91]
	s_add_u32 s13, s12, 3
	s_min_u32 s13, s13, 450
	s_cmp_ge_u32 s14, s13
	s_cbranch_scc0 .Lca_slow_3
.Lca_ok_1:
	buffer_load_dwordx4 v[42:45], v117, s[4:7], 0 offen offset:0 sc1
	ds_read_b128 v[50:53], v116 offset:256
	s_setprio 0
	v_exp_f32_e32 v94, v86
	v_exp_f32_e32 v95, v90
	v_exp_f32_e32 v96, v84
	v_exp_f32_e32 v97, v88
	v_exp_f32_e32 v98, v85
	v_exp_f32_e32 v99, v89
	v_pk_add_f32 v[100:101], v[94:95], 1.0 op_sel_hi:[1,0]
	v_pk_fma_f32 v[102:103], v[94:95], s[8:9], v[92:93] op_sel_hi:[1,0,0]
	v_pk_fma_f32 v[100:101], v[96:97], v[100:101], v[100:101]
	v_pk_fma_f32 v[104:105], v[100:101], v[98:99], v[100:101]
	v_rcp_f32_e32 v104, v104
	v_rcp_f32_e32 v105, v105
	v_pk_fma_f32 v[102:103], v[102:103], v[98:99], v[102:103]
	v_pk_fma_f32 v[102:103], v[64:65], v[100:101], v[102:103]
	v_exp_f32_e32 v106, v87
	v_pk_mul_f32 v[64:65], v[102:103], v[104:105]
	v_exp_f32_e32 v108, v64
	v_exp_f32_e32 v109, v65
	v_exp_f32_e32 v107, v91
	v_pk_add_f32 v[110:111], v[108:109], 1.0 op_sel_hi:[1,0]
	v_pk_fma_f32 v[110:111], v[110:111], v[106:107], v[110:111]
	v_rcp_f32_e32 v110, v110
	v_rcp_f32_e32 v111, v111
	v_pk_add_f32 v[112:113], v[108:109], -1.0 op_sel_hi:[1,0]
	v_pk_mul_f32 v[112:113], v[112:113], v[110:111]
	v_cvt_pk_f16_f32 v114, v112, v113
	ds_write_b32 v81, v114 offset:0
	s_waitcnt lgkmcnt(0)
	global_load_dword v67, v66, s[0:1] sc1
	global_load_dword v68, v66, s[0:1] offset:4 sc1
	s_setprio 2
	s_barrier
	v_mfma_f32_16x16x32_f16 v[84:87], v[6:9], v[50:53], v[18:21]
	v_mfma_f32_16x16x32_f16 v[88:91], v[10:13], v[50:53], v[38:41]
	ds_read_b128 v[56:59], v75 offset:0
	ds_read_b128 v[60:63], v75 offset:1024
	s_waitcnt vmcnt(3)
	v_mfma_f32_16x16x32_f16 v[84:87], v[2:5], v[46:49], v[84:87]
	v_mfma_f32_16x16x32_f16 v[88:91], v[14:17], v[46:49], v[88:91]
	s_waitcnt lgkmcnt(1)
	v_mfma_f32_16x16x32_f16 v[84:87], v[30:33], v[56:59], v[84:87]
	v_mfma_f32_16x16x32_f16 v[88:91], v[22:25], v[56:59], v[88:91]
	s_waitcnt lgkmcnt(0)
	v_mfma_f32_16x16x32_f16 v[84:87], v[34:37], v[60:63], v[84:87]
	v_mfma_f32_16x16x32_f16 v[88:91], v[26:29], v[60:63], v[88:91]
	s_add_u32 s13, s12, 4
	s_min_u32 s13, s13, 450
	s_cmp_ge_u32 s14, s13
	s_cbranch_scc0 .Lca_slow_6

.Lca_loop:
	s_setprio 2
	s_barrier
	v_mfma_f32_16x16x32_f16 v[84:87], v[6:9], v[50:53], v[18:21]
	v_mfma_f32_16x16x32_f16 v[88:91], v[10:13], v[50:53], v[38:41]
	ds_read_b128 v[56:59], v75 offset:2048
	ds_read_b128 v[60:63], v75 offset:3072
	s_waitcnt vmcnt(3)
	v_mfma_f32_16x16x32_f16 v[84:87], v[2:5], v[42:45], v[84:87]
	v_mfma_f32_16x16x32_f16 v[88:91], v[14:17], v[42:45], v[88:91]
	s_waitcnt lgkmcnt(1)
	v_mfma_f32_16x16x32_f16 v[84:87], v[30:33], v[56:59], v[84:87]
	v_mfma_f32_16x16x32_f16 v[88:91], v[22:25], v[56:59], v[88:91]
	s_waitcnt lgkmcnt(0)
	v_mfma_f32_16x16x32_f16 v[84:87], v[34:37], v[60:63], v[84:87]
	v_mfma_f32_16x16x32_f16 v[88:91], v[26:29], v[60:63], v[88:91]
	s_add_u32 s13, s12, 3
	s_min_u32 s13, s13, 450
	s_cmp_ge_u32 s14, s13
	s_cbranch_scc0 .Lca_slow_9
.Lca_ok_7:
	buffer_load_dwordx4 v[42:45], v117, s[4:7], 0 offen offset:0 sc1
	ds_read_b128 v[50:53], v116 offset:256
	s_setprio 0
	v_min_f32_e32 v64, 0x42700000, v64
	v_min_f32_e32 v65, 0x42700000, v65
	v_exp_f32_e32 v94, v86
	v_exp_f32_e32 v95, v90
	v_exp_f32_e32 v96, v84
	v_exp_f32_e32 v97, v88
	v_exp_f32_e32 v98, v85
	v_exp_f32_e32 v99, v89
	v_pk_add_f32 v[100:101], v[94:95], 1.0 op_sel_hi:[1,0]
	v_pk_fma_f32 v[102:103], v[94:95], s[8:9], v[92:93] op_sel_hi:[1,0,0]
	v_pk_fma_f32 v[100:101], v[96:97], v[100:101], v[100:101]
	v_pk_fma_f32 v[104:105], v[100:101], v[98:99], v[100:101]
	v_rcp_f32_e32 v104, v104
	v_rcp_f32_e32 v105, v105
	v_pk_fma_f32 v[102:103], v[102:103], v[98:99], v[102:103]
	v_pk_fma_f32 v[102:103], v[64:65], v[100:101], v[102:103]
	v_exp_f32_e32 v106, v87
	v_pk_mul_f32 v[64:65], v[102:103], v[104:105]
	v_exp_f32_e32 v108, v64
	v_exp_f32_e32 v109, v65
	v_exp_f32_e32 v107, v91
	v_pk_add_f32 v[110:111], v[108:109], 1.0 op_sel_hi:[1,0]
	v_pk_fma_f32 v[110:111], v[110:111], v[106:107], v[110:111]
	v_rcp_f32_e32 v110, v110
	v_rcp_f32_e32 v111, v111
	v_pk_add_f32 v[112:113], v[108:109], -1.0 op_sel_hi:[1,0]
	v_pk_mul_f32 v[112:113], v[112:113], v[110:111]
	v_cvt_pk_f16_f32 v114, v112, v113
	ds_write_b32 v81, v114 offset:0
	s_waitcnt lgkmcnt(0)
	s_waitcnt vmcnt(2)
	v_readfirstlane_b32 s10, v67
	v_readfirstlane_b32 s11, v68
	global_load_dword v67, v66, s[0:1] sc1
	global_load_dword v68, v66, s[0:1] offset:4 sc1
	s_min_u32 s10, s10, s11
	s_max_u32 s14, s14, s10
	s_setprio 2
	s_barrier
	v_mfma_f32_16x16x32_f16 v[84:87], v[6:9], v[50:53], v[18:21]
	v_mfma_f32_16x16x32_f16 v[88:91], v[10:13], v[50:53], v[38:41]
	ds_read_b128 v[56:59], v75 offset:0
	ds_read_b128 v[60:63], v75 offset:1024
	s_waitcnt vmcnt(3)
	v_mfma_f32_16x16x32_f16 v[84:87], v[2:5], v[46:49], v[84:87]
	v_mfma_f32_16x16x32_f16 v[88:91], v[14:17], v[46:49], v[88:91]
	s_waitcnt lgkmcnt(1)
	v_mfma_f32_16x16x32_f16 v[84:87], v[30:33], v[56:59], v[84:87]
	v_mfma_f32_16x16x32_f16 v[88:91], v[22:25], v[56:59], v[88:91]
	s_waitcnt lgkmcnt(0)
	v_mfma_f32_16x16x32_f16 v[84:87], v[34:37], v[60:63], v[84:87]
	v_mfma_f32_16x16x32_f16 v[88:91], v[26:29], v[60:63], v[88:91]
	s_add_u32 s13, s12, 4
	s_min_u32 s13, s13, 450
	s_cmp_ge_u32 s14, s13
	s_cbranch_scc0 .Lca_slow_12
.Lca_ok_10:
	buffer_load_dwordx4 v[46:49], v117, s[4:7], 0 offen offset:1024 sc1
	ds_read_b128 v[50:53], v116 offset:512
	s_setprio 0
	v_exp_f32_e32 v94, v86
	v_exp_f32_e32 v95, v90
	v_exp_f32_e32 v96, v84
	v_exp_f32_e32 v97, v88
	v_exp_f32_e32 v98, v85
	v_exp_f32_e32 v99, v89
	v_pk_add_f32 v[100:101], v[94:95], 1.0 op_sel_hi:[1,0]
	v_pk_fma_f32 v[102:103], v[94:95], s[8:9], v[92:93] op_sel_hi:[1,0,0]
	v_pk_fma_f32 v[100:101], v[96:97], v[100:101], v[100:101]
	v_pk_fma_f32 v[104:105], v[100:101], v[98:99], v[100:101]
	v_rcp_f32_e32 v104, v104
	v_rcp_f32_e32 v105, v105
	v_pk_fma_f32 v[102:103], v[102:103], v[98:99], v[102:103]
	v_pk_fma_f32 v[102:103], v[64:65], v[100:101], v[102:103]
	v_exp_f32_e32 v106, v87
	v_pk_mul_f32 v[64:65], v[102:103], v[104:105]
	v_exp_f32_e32 v108, v64
	v_exp_f32_e32 v109, v65
	v_exp_f32_e32 v107, v91
	v_pk_add_f32 v[110:111], v[108:109], 1.0 op_sel_hi:[1,0]
	v_pk_fma_f32 v[110:111], v[110:111], v[106:107], v[110:111]
	v_rcp_f32_e32 v110, v110
	v_rcp_f32_e32 v111, v111
	v_pk_add_f32 v[112:113], v[108:109], -1.0 op_sel_hi:[1,0]
	v_pk_mul_f32 v[112:113], v[112:113], v[110:111]
	v_cvt_pk_f16_f32 v114, v112, v113
	ds_write_b32 v81, v114 offset:2048
	s_waitcnt lgkmcnt(0)
	s_setprio 2
	s_barrier
	v_mfma_f32_16x16x32_f16 v[84:87], v[6:9], v[50:53], v[18:21]
	v_mfma_f32_16x16x32_f16 v[88:91], v[10:13], v[50:53], v[38:41]
	ds_read_b128 v[56:59], v75 offset:2048
	ds_read_b128 v[60:63], v75 offset:3072
	s_waitcnt vmcnt(3)
	v_mfma_f32_16x16x32_f16 v[84:87], v[2:5], v[42:45], v[84:87]
	v_mfma_f32_16x16x32_f16 v[88:91], v[14:17], v[42:45], v[88:91]
	s_waitcnt lgkmcnt(1)
	v_mfma_f32_16x16x32_f16 v[84:87], v[30:33], v[56:59], v[84:87]
	v_mfma_f32_16x16x32_f16 v[88:91], v[22:25], v[56:59], v[88:91]
	s_waitcnt lgkmcnt(0)
	v_mfma_f32_16x16x32_f16 v[84:87], v[34:37], v[60:63], v[84:87]
	v_mfma_f32_16x16x32_f16 v[88:91], v[26:29], v[60:63], v[88:91]
	s_add_u32 s13, s12, 5
	s_min_u32 s13, s13, 450
	s_cmp_ge_u32 s14, s13
	s_cbranch_scc0 .Lca_slow_15
.Lca_ok_13:
	buffer_load_dwordx4 v[42:45], v117, s[4:7], 0 offen offset:2048 sc1
	ds_read_b128 v[50:53], v116 offset:768
	s_setprio 0
	v_exp_f32_e32 v94, v86
	v_exp_f32_e32 v95, v90
	v_exp_f32_e32 v96, v84
	v_exp_f32_e32 v97, v88
	v_exp_f32_e32 v98, v85
	v_exp_f32_e32 v99, v89
	v_pk_add_f32 v[100:101], v[94:95], 1.0 op_sel_hi:[1,0]
	v_pk_fma_f32 v[102:103], v[94:95], s[8:9], v[92:93] op_sel_hi:[1,0,0]
	v_pk_fma_f32 v[100:101], v[96:97], v[100:101], v[100:101]
	v_pk_fma_f32 v[104:105], v[100:101], v[98:99], v[100:101]
	v_rcp_f32_e32 v104, v104
	v_rcp_f32_e32 v105, v105
	v_pk_fma_f32 v[102:103], v[102:103], v[98:99], v[102:103]
	v_pk_fma_f32 v[102:103], v[64:65], v[100:101], v[102:103]
	v_exp_f32_e32 v106, v87
	v_pk_mul_f32 v[64:65], v[102:103], v[104:105]
	v_exp_f32_e32 v108, v64
	v_exp_f32_e32 v109, v65
	v_exp_f32_e32 v107, v91
	v_pk_add_f32 v[110:111], v[108:109], 1.0 op_sel_hi:[1,0]
	v_pk_fma_f32 v[110:111], v[110:111], v[106:107], v[110:111]
	v_rcp_f32_e32 v110, v110
	v_rcp_f32_e32 v111, v111
	v_pk_add_f32 v[112:113], v[108:109], -1.0 op_sel_hi:[1,0]
	v_pk_mul_f32 v[112:113], v[112:113], v[110:111]
	v_cvt_pk_f16_f32 v114, v112, v113
	ds_write_b32 v81, v114 offset:0
	s_waitcnt lgkmcnt(0)
	s_waitcnt vmcnt(2)
	v_readfirstlane_b32 s10, v67
	v_readfirstlane_b32 s11, v68
	global_load_dword v67, v66, s[0:1] sc1
	global_load_dword v68, v66, s[0:1] offset:4 sc1
	s_min_u32 s10, s10, s11
	s_max_u32 s14, s14, s10
	s_setprio 2
	s_barrier
	v_mfma_f32_16x16x32_f16 v[84:87], v[6:9], v[50:53], v[18:21]
	v_mfma_f32_16x16x32_f16 v[88:91], v[10:13], v[50:53], v[38:41]
	ds_read_b128 v[56:59], v75 offset:0
	ds_read_b128 v[60:63], v75 offset:1024
	s_waitcnt vmcnt(3)
	v_mfma_f32_16x16x32_f16 v[84:87], v[2:5], v[46:49], v[84:87]
	v_mfma_f32_16x16x32_f16 v[88:91], v[14:17], v[46:49], v[88:91]
	s_waitcnt lgkmcnt(1)
	v_mfma_f32_16x16x32_f16 v[84:87], v[30:33], v[56:59], v[84:87]
	v_mfma_f32_16x16x32_f16 v[88:91], v[22:25], v[56:59], v[88:91]
	s_waitcnt lgkmcnt(0)
	v_mfma_f32_16x16x32_f16 v[84:87], v[34:37], v[60:63], v[84:87]
	v_mfma_f32_16x16x32_f16 v[88:91], v[26:29], v[60:63], v[88:91]
	s_add_u32 s13, s12, 6
	s_min_u32 s13, s13, 450
	s_cmp_ge_u32 s14, s13
	s_cbranch_scc0 .Lca_slow_18
